# fp8 K loops: the s_nop 1 wait states at the head of each MFMA cluster removed (operands come from LDS, not VALU)
# speedup vs baseline: 1.0011x; 1.0006x over previous
.LBB0_421:
	ds_read_b128 v[18:21], v196
	ds_read_b128 v[22:25], v196 offset:1024
	ds_read_b128 v[26:29], v196 offset:2048
	ds_read_b128 v[30:33], v196 offset:3072
	ds_read_b128 v[2:5], v197
	ds_read_b128 v[6:9], v197 offset:1024
	ds_read_b128 v[10:13], v197 offset:2048
	ds_read_b128 v[14:17], v197 offset:3072
	s_add_u32 s38, s36, 0x80
	s_addc_u32 s39, s37, 0
	s_cmp_eq_u32 s59, 12
	s_cselect_b32 s41, s29, s39
	s_cselect_b32 s40, s28, s38
	s_cselect_b32 s39, s31, s58
	s_cselect_b32 s38, s30, s27
	v_lshl_add_u64 v[224:225], s[36:37], 0, v[180:181]
	s_add_i32 m0, s35, 0xc000
	ds_read_b128 v[186:189], v198
	ds_read_b128 v[190:193], v198 offset:1024
	ds_read_b128 v[200:203], v198 offset:2048
	ds_read_b128 v[204:207], v198 offset:3072
	ds_read_b128 v[208:211], v198 offset:4096
	ds_read_b128 v[212:215], v198 offset:5120
	ds_read_b128 v[216:219], v198 offset:6144
	ds_read_b128 v[220:223], v198 offset:7168
	global_load_lds_dwordx4 v[224:225], off
	v_lshl_add_u64 v[224:225], s[36:37], 0, v[178:179]
	s_add_i32 m0, s35, 0xe000
	s_nop 0
	global_load_lds_dwordx4 v[224:225], off
	s_waitcnt vmcnt(8)
	s_waitcnt lgkmcnt(0)
	s_barrier
	s_setprio 1
	s_waitcnt lgkmcnt(0)
	v_mfma_f32_16x16x128_f8f6f4 v[158:161], v[18:25], v[186:193], v[158:161]
	v_mfma_f32_16x16x128_f8f6f4 v[154:157], v[26:33], v[186:193], v[154:157]
	v_mfma_f32_16x16x128_f8f6f4 v[142:145], v[18:25], v[200:207], v[142:145]
	v_mfma_f32_16x16x128_f8f6f4 v[138:141], v[26:33], v[200:207], v[138:141]
	v_mfma_f32_16x16x128_f8f6f4 v[126:129], v[18:25], v[208:215], v[126:129]
	v_mfma_f32_16x16x128_f8f6f4 v[122:125], v[26:33], v[208:215], v[122:125]
	v_mfma_f32_16x16x128_f8f6f4 v[110:113], v[18:25], v[216:223], v[110:113]
	v_mfma_f32_16x16x128_f8f6f4 v[106:109], v[26:33], v[216:223], v[106:109]
	s_setprio 0
	s_setprio 1
	v_mfma_f32_16x16x128_f8f6f4 v[150:153], v[2:9], v[186:193], v[150:153]
	v_mfma_f32_16x16x128_f8f6f4 v[146:149], v[10:17], v[186:193], v[146:149]
	v_mfma_f32_16x16x128_f8f6f4 v[134:137], v[2:9], v[200:207], v[134:137]
	v_mfma_f32_16x16x128_f8f6f4 v[130:133], v[10:17], v[200:207], v[130:133]
	v_mfma_f32_16x16x128_f8f6f4 v[118:121], v[2:9], v[208:215], v[118:121]
	v_mfma_f32_16x16x128_f8f6f4 v[114:117], v[10:17], v[208:215], v[114:117]
	v_mfma_f32_16x16x128_f8f6f4 v[102:105], v[2:9], v[216:223], v[102:105]
	v_mfma_f32_16x16x128_f8f6f4 v[98:101], v[10:17], v[216:223], v[98:101]
	s_setprio 0
	s_barrier
	s_add_i32 s60, s49, s42
	v_lshl_add_u64 v[186:187], s[38:39], 0, v[162:163]
	s_mov_b32 m0, s60
	ds_read_b128 v[200:203], v198 offset:16384
	ds_read_b128 v[204:207], v198 offset:17408
	ds_read_b128 v[208:211], v198 offset:18432
	ds_read_b128 v[212:215], v198 offset:19456
	ds_read_b128 v[216:219], v198 offset:20480
	ds_read_b128 v[220:223], v198 offset:21504
	ds_read_b128 v[230:233], v198 offset:22528
	ds_read_b128 v[234:237], v198 offset:23552
	global_load_lds_dwordx4 v[186:187], off
	s_add_i32 m0, s60, 0x2000
	s_add_u32 s60, s38, 0x40000
	v_lshl_add_u64 v[188:189], s[38:39], 0, v[164:165]
	s_addc_u32 s61, s39, 0
	s_add_i32 s62, s53, s42
	global_load_lds_dwordx4 v[188:189], off
	v_lshl_add_u64 v[190:191], s[60:61], 0, v[162:163]
	s_mov_b32 m0, s62
	v_lshl_add_u64 v[192:193], s[40:41], 0, v[168:169]
	global_load_lds_dwordx4 v[190:191], off
	v_lshl_add_u64 v[190:191], s[60:61], 0, v[164:165]
	s_add_i32 m0, s62, 0x2000
	s_nop 0
	global_load_lds_dwordx4 v[190:191], off
	v_lshl_add_u64 v[190:191], s[40:41], 0, v[166:167]
	s_mov_b32 m0, s35
	s_nop 0
	global_load_lds_dwordx4 v[190:191], off
	s_mov_b32 m0, s43
	s_nop 0
	global_load_lds_dwordx4 v[192:193], off
	s_waitcnt vmcnt(8)
	s_waitcnt lgkmcnt(0)
	s_barrier
	s_setprio 1
	s_waitcnt lgkmcnt(0)
	v_mfma_f32_16x16x128_f8f6f4 v[90:93], v[18:25], v[200:207], v[90:93]
	v_mfma_f32_16x16x128_f8f6f4 v[82:85], v[26:33], v[200:207], v[82:85]
	v_mfma_f32_16x16x128_f8f6f4 v[70:73], v[18:25], v[208:215], v[70:73]
	v_mfma_f32_16x16x128_f8f6f4 v[66:69], v[26:33], v[208:215], v[66:69]
	v_mfma_f32_16x16x128_f8f6f4 v[54:57], v[18:25], v[216:223], v[54:57]
	v_mfma_f32_16x16x128_f8f6f4 v[50:53], v[26:33], v[216:223], v[50:53]
	v_mfma_f32_16x16x128_f8f6f4 v[38:41], v[18:25], v[230:237], v[38:41]
	v_mfma_f32_16x16x128_f8f6f4 v[34:37], v[26:33], v[230:237], v[34:37]
	s_setprio 0
	s_setprio 1
	v_mfma_f32_16x16x128_f8f6f4 v[94:97], v[2:9], v[200:207], v[94:97]
	v_mfma_f32_16x16x128_f8f6f4 v[86:89], v[10:17], v[200:207], v[86:89]
	v_mfma_f32_16x16x128_f8f6f4 v[78:81], v[2:9], v[208:215], v[78:81]
	v_mfma_f32_16x16x128_f8f6f4 v[74:77], v[10:17], v[208:215], v[74:77]
	v_mfma_f32_16x16x128_f8f6f4 v[62:65], v[2:9], v[216:223], v[62:65]
	v_mfma_f32_16x16x128_f8f6f4 v[58:61], v[10:17], v[216:223], v[58:61]
	v_mfma_f32_16x16x128_f8f6f4 v[46:49], v[2:9], v[230:237], v[46:49]
	v_mfma_f32_16x16x128_f8f6f4 v[42:45], v[10:17], v[230:237], v[42:45]
	s_setprio 0
	s_barrier
	s_add_i32 s60, 0, 0x18000
	s_add_i32 s61, 0, 0x1c000
	v_add_u32_e32 v14, s60, v194
	v_add_u32_e32 v30, s61, v194
	ds_read_b128 v[2:5], v14
	ds_read_b128 v[6:9], v14 offset:1024
	ds_read_b128 v[10:13], v14 offset:2048
	ds_read_b128 v[14:17], v14 offset:3072
	ds_read_b128 v[18:21], v30
	ds_read_b128 v[22:25], v30 offset:1024
	ds_read_b128 v[26:29], v30 offset:2048
	ds_read_b128 v[30:33], v30 offset:3072
	s_mov_b32 m0, s44
	v_lshl_add_u64 v[224:225], s[40:41], 0, v[170:171]
	ds_read_b128 v[200:203], v198 offset:32768
	ds_read_b128 v[204:207], v198 offset:33792
	ds_read_b128 v[208:211], v198 offset:34816
	ds_read_b128 v[212:215], v198 offset:35840
	ds_read_b128 v[216:219], v198 offset:36864
	ds_read_b128 v[220:223], v198 offset:37888
	ds_read_b128 v[230:233], v198 offset:38912
	ds_read_b128 v[234:237], v198 offset:39936
	global_load_lds_dwordx4 v[224:225], off
	v_lshl_add_u64 v[224:225], s[40:41], 0, v[172:173]
	s_mov_b32 m0, s45
	s_nop 0
	global_load_lds_dwordx4 v[224:225], off
	s_waitcnt vmcnt(8)
	s_waitcnt lgkmcnt(0)
	s_barrier
	s_setprio 1
	s_waitcnt lgkmcnt(0)
	v_mfma_f32_16x16x128_f8f6f4 v[158:161], v[2:9], v[200:207], v[158:161]
	v_mfma_f32_16x16x128_f8f6f4 v[154:157], v[10:17], v[200:207], v[154:157]
	v_mfma_f32_16x16x128_f8f6f4 v[142:145], v[2:9], v[208:215], v[142:145]
	v_mfma_f32_16x16x128_f8f6f4 v[138:141], v[10:17], v[208:215], v[138:141]
	v_mfma_f32_16x16x128_f8f6f4 v[126:129], v[2:9], v[216:223], v[126:129]
	v_mfma_f32_16x16x128_f8f6f4 v[122:125], v[10:17], v[216:223], v[122:125]
	v_mfma_f32_16x16x128_f8f6f4 v[110:113], v[2:9], v[230:237], v[110:113]
	v_mfma_f32_16x16x128_f8f6f4 v[106:109], v[10:17], v[230:237], v[106:109]
	s_setprio 0
	s_setprio 1
	v_mfma_f32_16x16x128_f8f6f4 v[150:153], v[18:25], v[200:207], v[150:153]
	v_mfma_f32_16x16x128_f8f6f4 v[146:149], v[26:33], v[200:207], v[146:149]
	v_mfma_f32_16x16x128_f8f6f4 v[134:137], v[18:25], v[208:215], v[134:137]
	v_mfma_f32_16x16x128_f8f6f4 v[130:133], v[26:33], v[208:215], v[130:133]
	v_mfma_f32_16x16x128_f8f6f4 v[118:121], v[18:25], v[216:223], v[118:121]
	v_mfma_f32_16x16x128_f8f6f4 v[114:117], v[26:33], v[216:223], v[114:117]
	v_mfma_f32_16x16x128_f8f6f4 v[102:105], v[18:25], v[230:237], v[102:105]
	v_mfma_f32_16x16x128_f8f6f4 v[98:101], v[26:33], v[230:237], v[98:101]
	s_setprio 0
	s_barrier
	s_add_i32 s40, s60, s42
	v_lshl_add_u64 v[186:187], v[186:187], 0, s[14:15]
	s_mov_b32 m0, s40
	ds_read_b128 v[200:203], v198 offset:49152
	ds_read_b128 v[204:207], v198 offset:50176
	ds_read_b128 v[208:211], v198 offset:51200
	ds_read_b128 v[212:215], v198 offset:52224
	ds_read_b128 v[216:219], v198 offset:53248
	ds_read_b128 v[220:223], v198 offset:54272
	ds_read_b128 v[230:233], v198 offset:55296
	ds_read_b128 v[234:237], v198 offset:56320
	global_load_lds_dwordx4 v[186:187], off
	s_add_i32 m0, s40, 0x2000
	s_add_u32 s38, s38, 0x40080
	v_lshl_add_u64 v[186:187], v[188:189], 0, s[14:15]
	s_addc_u32 s39, s39, 0
	s_add_i32 s40, s61, s42
	global_load_lds_dwordx4 v[186:187], off
	v_lshl_add_u64 v[186:187], s[38:39], 0, v[162:163]
	s_mov_b32 m0, s40
	s_nop 0
	global_load_lds_dwordx4 v[186:187], off
	v_lshl_add_u64 v[186:187], s[38:39], 0, v[164:165]
	s_add_i32 m0, s40, 0x2000
	s_nop 0
	global_load_lds_dwordx4 v[186:187], off
	v_lshl_add_u64 v[186:187], v[190:191], 0, s[14:15]
	s_mov_b32 m0, s46
	s_nop 0
	global_load_lds_dwordx4 v[186:187], off
	v_lshl_add_u64 v[186:187], v[192:193], 0, s[14:15]
	s_mov_b32 m0, s47
	s_nop 0
	global_load_lds_dwordx4 v[186:187], off
	s_waitcnt vmcnt(8)
	s_waitcnt lgkmcnt(0)
	s_barrier
	s_setprio 1
	s_waitcnt lgkmcnt(0)
	v_mfma_f32_16x16x128_f8f6f4 v[90:93], v[2:9], v[200:207], v[90:93]
	v_mfma_f32_16x16x128_f8f6f4 v[82:85], v[10:17], v[200:207], v[82:85]
	v_mfma_f32_16x16x128_f8f6f4 v[70:73], v[2:9], v[208:215], v[70:73]
	v_mfma_f32_16x16x128_f8f6f4 v[66:69], v[10:17], v[208:215], v[66:69]
	v_mfma_f32_16x16x128_f8f6f4 v[54:57], v[2:9], v[216:223], v[54:57]
	v_mfma_f32_16x16x128_f8f6f4 v[50:53], v[10:17], v[216:223], v[50:53]
	v_mfma_f32_16x16x128_f8f6f4 v[38:41], v[2:9], v[230:237], v[38:41]
	v_mfma_f32_16x16x128_f8f6f4 v[34:37], v[10:17], v[230:237], v[34:37]
	s_setprio 0
	s_setprio 1
	v_mfma_f32_16x16x128_f8f6f4 v[94:97], v[18:25], v[200:207], v[94:97]
	v_mfma_f32_16x16x128_f8f6f4 v[86:89], v[26:33], v[200:207], v[86:89]
	v_mfma_f32_16x16x128_f8f6f4 v[78:81], v[18:25], v[208:215], v[78:81]
	v_mfma_f32_16x16x128_f8f6f4 v[74:77], v[26:33], v[208:215], v[74:77]
	v_mfma_f32_16x16x128_f8f6f4 v[62:65], v[18:25], v[216:223], v[62:65]
	v_mfma_f32_16x16x128_f8f6f4 v[58:61], v[26:33], v[216:223], v[58:61]
	v_mfma_f32_16x16x128_f8f6f4 v[46:49], v[18:25], v[230:237], v[46:49]
	v_mfma_f32_16x16x128_f8f6f4 v[42:45], v[26:33], v[230:237], v[42:45]
	s_setprio 0
	s_barrier
	s_add_i32 s59, s59, 2
	s_add_u32 s36, s36, 0x100
	s_addc_u32 s37, s37, 0
	s_add_u32 s27, s27, 0x100
	s_addc_u32 s58, s58, 0
	s_cmp_gt_u32 s59, 13
	s_cbranch_scc0 .LBB0_421
	s_and_b64 vcc, exec, s[2:3]
	s_cbranch_vccz .LBB0_424
	s_barrier

.LBB0_459:
	s_and_b64 s[46:47], s[38:39], exec
	s_cselect_b32 s48, s35, s43
	s_cselect_b32 s49, s34, s42
	s_cselect_b32 s66, s37, s45
	s_cselect_b32 s67, s36, s44
	s_add_u32 s42, s42, 0x80
	s_addc_u32 s43, s43, 0
	s_add_u32 s68, s44, 0x100
	s_addc_u32 s69, s45, 0
	s_mov_b32 s70, -2
	ds_read_b128 v[18:21], v194
	ds_read_b128 v[22:25], v194 offset:1024
	ds_read_b128 v[26:29], v194 offset:2048
	ds_read_b128 v[30:33], v194 offset:3072
	ds_read_b128 v[2:5], v195
	ds_read_b128 v[6:9], v195 offset:1024
	ds_read_b128 v[10:13], v195 offset:2048
	ds_read_b128 v[14:17], v195 offset:3072
	s_add_u32 s44, s42, 0x80
	s_addc_u32 s45, s43, 0
	s_cmp_eq_u32 s70, 12
	s_cselect_b32 s47, s48, s45
	s_cselect_b32 s46, s49, s44
	s_cselect_b32 s45, s66, s69
	s_cselect_b32 s44, s67, s68
	v_lshl_add_u64 v[222:223], s[42:43], 0, v[180:181]
	s_add_i32 m0, s41, 0xc000
	ds_read_b128 v[184:187], v196
	ds_read_b128 v[188:191], v196 offset:1024
	ds_read_b128 v[198:201], v196 offset:2048
	ds_read_b128 v[202:205], v196 offset:3072
	ds_read_b128 v[206:209], v196 offset:4096
	ds_read_b128 v[210:213], v196 offset:5120
	ds_read_b128 v[214:217], v196 offset:6144
	ds_read_b128 v[218:221], v196 offset:7168
	global_load_lds_dwordx4 v[222:223], off
	v_lshl_add_u64 v[222:223], s[42:43], 0, v[178:179]
	s_add_i32 m0, s41, 0xe000
	s_nop 0
	global_load_lds_dwordx4 v[222:223], off
	s_waitcnt vmcnt(8)
	s_waitcnt lgkmcnt(0)
	s_barrier
	s_setprio 1
	s_waitcnt lgkmcnt(0)
	v_mfma_f32_16x16x128_f8f6f4 v[158:161], v[18:25], v[184:191], 0
	v_mfma_f32_16x16x128_f8f6f4 v[154:157], v[26:33], v[184:191], 0
	v_mfma_f32_16x16x128_f8f6f4 v[142:145], v[18:25], v[198:205], 0
	v_mfma_f32_16x16x128_f8f6f4 v[138:141], v[26:33], v[198:205], 0
	v_mfma_f32_16x16x128_f8f6f4 v[126:129], v[18:25], v[206:213], 0
	v_mfma_f32_16x16x128_f8f6f4 v[122:125], v[26:33], v[206:213], 0
	v_mfma_f32_16x16x128_f8f6f4 v[110:113], v[18:25], v[214:221], 0
	v_mfma_f32_16x16x128_f8f6f4 v[106:109], v[26:33], v[214:221], 0
	s_setprio 0
	s_setprio 1
	v_mfma_f32_16x16x128_f8f6f4 v[150:153], v[2:9], v[184:191], 0
	v_mfma_f32_16x16x128_f8f6f4 v[146:149], v[10:17], v[184:191], 0
	v_mfma_f32_16x16x128_f8f6f4 v[134:137], v[2:9], v[198:205], 0
	v_mfma_f32_16x16x128_f8f6f4 v[130:133], v[10:17], v[198:205], 0
	v_mfma_f32_16x16x128_f8f6f4 v[118:121], v[2:9], v[206:213], 0
	v_mfma_f32_16x16x128_f8f6f4 v[114:117], v[10:17], v[206:213], 0
	v_mfma_f32_16x16x128_f8f6f4 v[102:105], v[2:9], v[214:221], 0
	v_mfma_f32_16x16x128_f8f6f4 v[98:101], v[10:17], v[214:221], 0
	s_setprio 0
	s_barrier
	s_add_i32 s71, s61, s53
	v_lshl_add_u64 v[184:185], s[44:45], 0, v[162:163]
	s_mov_b32 m0, s71
	ds_read_b128 v[198:201], v196 offset:16384
	ds_read_b128 v[202:205], v196 offset:17408
	ds_read_b128 v[206:209], v196 offset:18432
	ds_read_b128 v[210:213], v196 offset:19456
	ds_read_b128 v[214:217], v196 offset:20480
	ds_read_b128 v[218:221], v196 offset:21504
	ds_read_b128 v[230:233], v196 offset:22528
	ds_read_b128 v[234:237], v196 offset:23552
	global_load_lds_dwordx4 v[184:185], off
	s_add_i32 m0, s71, 0x2000
	s_add_u32 s72, s44, 0x40000
	v_lshl_add_u64 v[186:187], s[44:45], 0, v[164:165]
	s_addc_u32 s73, s45, 0
	s_add_i32 s71, s62, s53
	global_load_lds_dwordx4 v[186:187], off
	v_lshl_add_u64 v[188:189], s[72:73], 0, v[162:163]
	s_mov_b32 m0, s71
	v_lshl_add_u64 v[190:191], s[46:47], 0, v[168:169]
	global_load_lds_dwordx4 v[188:189], off
	v_lshl_add_u64 v[188:189], s[72:73], 0, v[164:165]
	s_add_i32 m0, s71, 0x2000
	s_nop 0
	global_load_lds_dwordx4 v[188:189], off
	v_lshl_add_u64 v[188:189], s[46:47], 0, v[166:167]
	s_mov_b32 m0, s41
	s_nop 0
	global_load_lds_dwordx4 v[188:189], off
	s_mov_b32 m0, s54
	s_nop 0
	global_load_lds_dwordx4 v[190:191], off
	s_waitcnt vmcnt(8)
	s_waitcnt lgkmcnt(0)
	s_barrier
	s_setprio 1
	s_waitcnt lgkmcnt(0)
	v_mfma_f32_16x16x128_f8f6f4 v[90:93], v[18:25], v[198:205], 0
	v_mfma_f32_16x16x128_f8f6f4 v[82:85], v[26:33], v[198:205], 0
	v_mfma_f32_16x16x128_f8f6f4 v[70:73], v[18:25], v[206:213], 0
	v_mfma_f32_16x16x128_f8f6f4 v[66:69], v[26:33], v[206:213], 0
	v_mfma_f32_16x16x128_f8f6f4 v[54:57], v[18:25], v[214:221], 0
	v_mfma_f32_16x16x128_f8f6f4 v[50:53], v[26:33], v[214:221], 0
	v_mfma_f32_16x16x128_f8f6f4 v[38:41], v[18:25], v[230:237], 0
	v_mfma_f32_16x16x128_f8f6f4 v[34:37], v[26:33], v[230:237], 0
	s_setprio 0
	s_setprio 1
	v_mfma_f32_16x16x128_f8f6f4 v[94:97], v[2:9], v[198:205], 0
	v_mfma_f32_16x16x128_f8f6f4 v[86:89], v[10:17], v[198:205], 0
	v_mfma_f32_16x16x128_f8f6f4 v[78:81], v[2:9], v[206:213], 0
	v_mfma_f32_16x16x128_f8f6f4 v[74:77], v[10:17], v[206:213], 0
	v_mfma_f32_16x16x128_f8f6f4 v[62:65], v[2:9], v[214:221], 0
	v_mfma_f32_16x16x128_f8f6f4 v[58:61], v[10:17], v[214:221], 0
	v_mfma_f32_16x16x128_f8f6f4 v[46:49], v[2:9], v[230:237], 0
	v_mfma_f32_16x16x128_f8f6f4 v[42:45], v[10:17], v[230:237], 0
	s_setprio 0
	s_barrier
	s_add_i32 s71, 0, 0x18000
	s_add_i32 s72, 0, 0x1c000
	v_add_u32_e32 v14, s71, v192
	v_add_u32_e32 v30, s72, v192
	ds_read_b128 v[2:5], v14
	ds_read_b128 v[6:9], v14 offset:1024
	ds_read_b128 v[10:13], v14 offset:2048
	ds_read_b128 v[14:17], v14 offset:3072
	ds_read_b128 v[18:21], v30
	ds_read_b128 v[22:25], v30 offset:1024
	ds_read_b128 v[26:29], v30 offset:2048
	ds_read_b128 v[30:33], v30 offset:3072
	s_mov_b32 m0, s55
	v_lshl_add_u64 v[222:223], s[46:47], 0, v[170:171]
	ds_read_b128 v[198:201], v196 offset:32768
	ds_read_b128 v[202:205], v196 offset:33792
	ds_read_b128 v[206:209], v196 offset:34816
	ds_read_b128 v[210:213], v196 offset:35840
	ds_read_b128 v[214:217], v196 offset:36864
	ds_read_b128 v[218:221], v196 offset:37888
	ds_read_b128 v[230:233], v196 offset:38912
	ds_read_b128 v[234:237], v196 offset:39936
	global_load_lds_dwordx4 v[222:223], off
	v_lshl_add_u64 v[222:223], s[46:47], 0, v[172:173]
	s_mov_b32 m0, s58
	s_nop 0
	global_load_lds_dwordx4 v[222:223], off
	s_waitcnt vmcnt(8)
	s_waitcnt lgkmcnt(0)
	s_barrier
	s_setprio 1
	s_waitcnt lgkmcnt(0)
	v_mfma_f32_16x16x128_f8f6f4 v[158:161], v[2:9], v[198:205], v[158:161]
	v_mfma_f32_16x16x128_f8f6f4 v[154:157], v[10:17], v[198:205], v[154:157]
	v_mfma_f32_16x16x128_f8f6f4 v[142:145], v[2:9], v[206:213], v[142:145]
	v_mfma_f32_16x16x128_f8f6f4 v[138:141], v[10:17], v[206:213], v[138:141]
	v_mfma_f32_16x16x128_f8f6f4 v[126:129], v[2:9], v[214:221], v[126:129]
	v_mfma_f32_16x16x128_f8f6f4 v[122:125], v[10:17], v[214:221], v[122:125]
	v_mfma_f32_16x16x128_f8f6f4 v[110:113], v[2:9], v[230:237], v[110:113]
	v_mfma_f32_16x16x128_f8f6f4 v[106:109], v[10:17], v[230:237], v[106:109]
	s_setprio 0
	s_setprio 1
	v_mfma_f32_16x16x128_f8f6f4 v[150:153], v[18:25], v[198:205], v[150:153]
	v_mfma_f32_16x16x128_f8f6f4 v[146:149], v[26:33], v[198:205], v[146:149]
	v_mfma_f32_16x16x128_f8f6f4 v[134:137], v[18:25], v[206:213], v[134:137]
	v_mfma_f32_16x16x128_f8f6f4 v[130:133], v[26:33], v[206:213], v[130:133]
	v_mfma_f32_16x16x128_f8f6f4 v[118:121], v[18:25], v[214:221], v[118:121]
	v_mfma_f32_16x16x128_f8f6f4 v[114:117], v[26:33], v[214:221], v[114:117]
	v_mfma_f32_16x16x128_f8f6f4 v[102:105], v[18:25], v[230:237], v[102:105]
	v_mfma_f32_16x16x128_f8f6f4 v[98:101], v[26:33], v[230:237], v[98:101]
	s_setprio 0
	s_barrier
	s_add_i32 s46, s71, s53
	v_lshl_add_u64 v[184:185], v[184:185], 0, s[12:13]
	s_mov_b32 m0, s46
	ds_read_b128 v[198:201], v196 offset:49152
	ds_read_b128 v[202:205], v196 offset:50176
	ds_read_b128 v[206:209], v196 offset:51200
	ds_read_b128 v[210:213], v196 offset:52224
	ds_read_b128 v[214:217], v196 offset:53248
	ds_read_b128 v[218:221], v196 offset:54272
	ds_read_b128 v[230:233], v196 offset:55296
	ds_read_b128 v[234:237], v196 offset:56320
	global_load_lds_dwordx4 v[184:185], off
	s_add_i32 m0, s46, 0x2000
	s_add_u32 s44, s44, 0x40080
	v_lshl_add_u64 v[184:185], v[186:187], 0, s[12:13]
	s_addc_u32 s45, s45, 0
	s_add_i32 s46, s72, s53
	global_load_lds_dwordx4 v[184:185], off
	v_lshl_add_u64 v[184:185], s[44:45], 0, v[162:163]
	s_mov_b32 m0, s46
	s_nop 0
	global_load_lds_dwordx4 v[184:185], off
	v_lshl_add_u64 v[184:185], s[44:45], 0, v[164:165]
	s_add_i32 m0, s46, 0x2000
	s_nop 0
	global_load_lds_dwordx4 v[184:185], off
	v_lshl_add_u64 v[184:185], v[188:189], 0, s[12:13]
	s_mov_b32 m0, s59
	s_nop 0
	global_load_lds_dwordx4 v[184:185], off
	v_lshl_add_u64 v[184:185], v[190:191], 0, s[12:13]
	s_mov_b32 m0, s60
	s_nop 0
	global_load_lds_dwordx4 v[184:185], off
	s_waitcnt vmcnt(8)
	s_waitcnt lgkmcnt(0)
	s_barrier
	s_setprio 1
	s_waitcnt lgkmcnt(0)
	v_mfma_f32_16x16x128_f8f6f4 v[90:93], v[2:9], v[198:205], v[90:93]
	v_mfma_f32_16x16x128_f8f6f4 v[82:85], v[10:17], v[198:205], v[82:85]
	v_mfma_f32_16x16x128_f8f6f4 v[70:73], v[2:9], v[206:213], v[70:73]
	v_mfma_f32_16x16x128_f8f6f4 v[66:69], v[10:17], v[206:213], v[66:69]
	v_mfma_f32_16x16x128_f8f6f4 v[54:57], v[2:9], v[214:221], v[54:57]
	v_mfma_f32_16x16x128_f8f6f4 v[50:53], v[10:17], v[214:221], v[50:53]
	v_mfma_f32_16x16x128_f8f6f4 v[38:41], v[2:9], v[230:237], v[38:41]
	v_mfma_f32_16x16x128_f8f6f4 v[34:37], v[10:17], v[230:237], v[34:37]
	s_setprio 0
	s_setprio 1
	v_mfma_f32_16x16x128_f8f6f4 v[94:97], v[18:25], v[198:205], v[94:97]
	v_mfma_f32_16x16x128_f8f6f4 v[86:89], v[26:33], v[198:205], v[86:89]
	v_mfma_f32_16x16x128_f8f6f4 v[78:81], v[18:25], v[206:213], v[78:81]
	v_mfma_f32_16x16x128_f8f6f4 v[74:77], v[26:33], v[206:213], v[74:77]
	v_mfma_f32_16x16x128_f8f6f4 v[62:65], v[18:25], v[214:221], v[62:65]
	v_mfma_f32_16x16x128_f8f6f4 v[58:61], v[26:33], v[214:221], v[58:61]
	v_mfma_f32_16x16x128_f8f6f4 v[46:49], v[18:25], v[230:237], v[46:49]
	v_mfma_f32_16x16x128_f8f6f4 v[42:45], v[26:33], v[230:237], v[42:45]
	s_setprio 0
	s_barrier
	s_add_i32 s70, s70, 2
	s_add_u32 s42, s42, 0x100
	s_addc_u32 s43, s43, 0
	s_add_u32 s68, s68, 0x100
	s_addc_u32 s69, s69, 0
	s_cmp_gt_u32 s70, 13
	s_cbranch_scc0 .LBB0_460
	s_branch .Lmy_pexit_p1b
.LBB0_460:
	ds_read_b128 v[18:21], v194
	ds_read_b128 v[22:25], v194 offset:1024
	ds_read_b128 v[26:29], v194 offset:2048
	ds_read_b128 v[30:33], v194 offset:3072
	ds_read_b128 v[2:5], v195
	ds_read_b128 v[6:9], v195 offset:1024
	ds_read_b128 v[10:13], v195 offset:2048
	ds_read_b128 v[14:17], v195 offset:3072
	s_add_u32 s44, s42, 0x80
	s_addc_u32 s45, s43, 0
	s_cmp_eq_u32 s70, 12
	s_cselect_b32 s47, s48, s45
	s_cselect_b32 s46, s49, s44
	s_cselect_b32 s45, s66, s69
	s_cselect_b32 s44, s67, s68
	v_lshl_add_u64 v[222:223], s[42:43], 0, v[180:181]
	s_add_i32 m0, s41, 0xc000
	ds_read_b128 v[184:187], v196
	ds_read_b128 v[188:191], v196 offset:1024
	ds_read_b128 v[198:201], v196 offset:2048
	ds_read_b128 v[202:205], v196 offset:3072
	ds_read_b128 v[206:209], v196 offset:4096
	ds_read_b128 v[210:213], v196 offset:5120
	ds_read_b128 v[214:217], v196 offset:6144
	ds_read_b128 v[218:221], v196 offset:7168
	global_load_lds_dwordx4 v[222:223], off
	v_lshl_add_u64 v[222:223], s[42:43], 0, v[178:179]
	s_add_i32 m0, s41, 0xe000
	s_nop 0
	global_load_lds_dwordx4 v[222:223], off
	s_waitcnt vmcnt(8)
	s_waitcnt lgkmcnt(0)
	s_barrier
	s_setprio 1
	s_waitcnt lgkmcnt(0)
	v_mfma_f32_16x16x128_f8f6f4 v[158:161], v[18:25], v[184:191], v[158:161]
	v_mfma_f32_16x16x128_f8f6f4 v[154:157], v[26:33], v[184:191], v[154:157]
	v_mfma_f32_16x16x128_f8f6f4 v[142:145], v[18:25], v[198:205], v[142:145]
	v_mfma_f32_16x16x128_f8f6f4 v[138:141], v[26:33], v[198:205], v[138:141]
	v_mfma_f32_16x16x128_f8f6f4 v[126:129], v[18:25], v[206:213], v[126:129]
	v_mfma_f32_16x16x128_f8f6f4 v[122:125], v[26:33], v[206:213], v[122:125]
	v_mfma_f32_16x16x128_f8f6f4 v[110:113], v[18:25], v[214:221], v[110:113]
	v_mfma_f32_16x16x128_f8f6f4 v[106:109], v[26:33], v[214:221], v[106:109]
	s_setprio 0
	s_setprio 1
	v_mfma_f32_16x16x128_f8f6f4 v[150:153], v[2:9], v[184:191], v[150:153]
	v_mfma_f32_16x16x128_f8f6f4 v[146:149], v[10:17], v[184:191], v[146:149]
	v_mfma_f32_16x16x128_f8f6f4 v[134:137], v[2:9], v[198:205], v[134:137]
	v_mfma_f32_16x16x128_f8f6f4 v[130:133], v[10:17], v[198:205], v[130:133]
	v_mfma_f32_16x16x128_f8f6f4 v[118:121], v[2:9], v[206:213], v[118:121]
	v_mfma_f32_16x16x128_f8f6f4 v[114:117], v[10:17], v[206:213], v[114:117]
	v_mfma_f32_16x16x128_f8f6f4 v[102:105], v[2:9], v[214:221], v[102:105]
	v_mfma_f32_16x16x128_f8f6f4 v[98:101], v[10:17], v[214:221], v[98:101]
	s_setprio 0
	s_barrier
	s_add_i32 s71, s61, s53
	v_lshl_add_u64 v[184:185], s[44:45], 0, v[162:163]
	s_mov_b32 m0, s71
	ds_read_b128 v[198:201], v196 offset:16384
	ds_read_b128 v[202:205], v196 offset:17408
	ds_read_b128 v[206:209], v196 offset:18432
	ds_read_b128 v[210:213], v196 offset:19456
	ds_read_b128 v[214:217], v196 offset:20480
	ds_read_b128 v[218:221], v196 offset:21504
	ds_read_b128 v[230:233], v196 offset:22528
	ds_read_b128 v[234:237], v196 offset:23552
	global_load_lds_dwordx4 v[184:185], off
	s_add_i32 m0, s71, 0x2000
	s_add_u32 s72, s44, 0x40000
	v_lshl_add_u64 v[186:187], s[44:45], 0, v[164:165]
	s_addc_u32 s73, s45, 0
	s_add_i32 s71, s62, s53
	global_load_lds_dwordx4 v[186:187], off
	v_lshl_add_u64 v[188:189], s[72:73], 0, v[162:163]
	s_mov_b32 m0, s71
	v_lshl_add_u64 v[190:191], s[46:47], 0, v[168:169]
	global_load_lds_dwordx4 v[188:189], off
	v_lshl_add_u64 v[188:189], s[72:73], 0, v[164:165]
	s_add_i32 m0, s71, 0x2000
	s_nop 0
	global_load_lds_dwordx4 v[188:189], off
	v_lshl_add_u64 v[188:189], s[46:47], 0, v[166:167]
	s_mov_b32 m0, s41
	s_nop 0
	global_load_lds_dwordx4 v[188:189], off
	s_mov_b32 m0, s54
	s_nop 0
	global_load_lds_dwordx4 v[190:191], off
	s_waitcnt vmcnt(8)
	s_waitcnt lgkmcnt(0)
	s_barrier
	s_setprio 1
	s_waitcnt lgkmcnt(0)
	v_mfma_f32_16x16x128_f8f6f4 v[90:93], v[18:25], v[198:205], v[90:93]
	v_mfma_f32_16x16x128_f8f6f4 v[82:85], v[26:33], v[198:205], v[82:85]
	v_mfma_f32_16x16x128_f8f6f4 v[70:73], v[18:25], v[206:213], v[70:73]
	v_mfma_f32_16x16x128_f8f6f4 v[66:69], v[26:33], v[206:213], v[66:69]
	v_mfma_f32_16x16x128_f8f6f4 v[54:57], v[18:25], v[214:221], v[54:57]
	v_mfma_f32_16x16x128_f8f6f4 v[50:53], v[26:33], v[214:221], v[50:53]
	v_mfma_f32_16x16x128_f8f6f4 v[38:41], v[18:25], v[230:237], v[38:41]
	v_mfma_f32_16x16x128_f8f6f4 v[34:37], v[26:33], v[230:237], v[34:37]
	s_setprio 0
	s_setprio 1
	v_mfma_f32_16x16x128_f8f6f4 v[94:97], v[2:9], v[198:205], v[94:97]
	v_mfma_f32_16x16x128_f8f6f4 v[86:89], v[10:17], v[198:205], v[86:89]
	v_mfma_f32_16x16x128_f8f6f4 v[78:81], v[2:9], v[206:213], v[78:81]
	v_mfma_f32_16x16x128_f8f6f4 v[74:77], v[10:17], v[206:213], v[74:77]
	v_mfma_f32_16x16x128_f8f6f4 v[62:65], v[2:9], v[214:221], v[62:65]
	v_mfma_f32_16x16x128_f8f6f4 v[58:61], v[10:17], v[214:221], v[58:61]
	v_mfma_f32_16x16x128_f8f6f4 v[46:49], v[2:9], v[230:237], v[46:49]
	v_mfma_f32_16x16x128_f8f6f4 v[42:45], v[10:17], v[230:237], v[42:45]
	s_setprio 0
	s_barrier
	s_add_i32 s71, 0, 0x18000
	s_add_i32 s72, 0, 0x1c000
	v_add_u32_e32 v14, s71, v192
	v_add_u32_e32 v30, s72, v192
	ds_read_b128 v[2:5], v14
	ds_read_b128 v[6:9], v14 offset:1024
	ds_read_b128 v[10:13], v14 offset:2048
	ds_read_b128 v[14:17], v14 offset:3072
	ds_read_b128 v[18:21], v30
	ds_read_b128 v[22:25], v30 offset:1024
	ds_read_b128 v[26:29], v30 offset:2048
	ds_read_b128 v[30:33], v30 offset:3072
	s_mov_b32 m0, s55
	v_lshl_add_u64 v[222:223], s[46:47], 0, v[170:171]
	ds_read_b128 v[198:201], v196 offset:32768
	ds_read_b128 v[202:205], v196 offset:33792
	ds_read_b128 v[206:209], v196 offset:34816
	ds_read_b128 v[210:213], v196 offset:35840
	ds_read_b128 v[214:217], v196 offset:36864
	ds_read_b128 v[218:221], v196 offset:37888
	ds_read_b128 v[230:233], v196 offset:38912
	ds_read_b128 v[234:237], v196 offset:39936
	global_load_lds_dwordx4 v[222:223], off
	v_lshl_add_u64 v[222:223], s[46:47], 0, v[172:173]
	s_mov_b32 m0, s58
	s_nop 0
	global_load_lds_dwordx4 v[222:223], off
	s_waitcnt vmcnt(8)
	s_waitcnt lgkmcnt(0)
	s_barrier
	s_setprio 1
	s_waitcnt lgkmcnt(0)
	v_mfma_f32_16x16x128_f8f6f4 v[158:161], v[2:9], v[198:205], v[158:161]
	v_mfma_f32_16x16x128_f8f6f4 v[154:157], v[10:17], v[198:205], v[154:157]
	v_mfma_f32_16x16x128_f8f6f4 v[142:145], v[2:9], v[206:213], v[142:145]
	v_mfma_f32_16x16x128_f8f6f4 v[138:141], v[10:17], v[206:213], v[138:141]
	v_mfma_f32_16x16x128_f8f6f4 v[126:129], v[2:9], v[214:221], v[126:129]
	v_mfma_f32_16x16x128_f8f6f4 v[122:125], v[10:17], v[214:221], v[122:125]
	v_mfma_f32_16x16x128_f8f6f4 v[110:113], v[2:9], v[230:237], v[110:113]
	v_mfma_f32_16x16x128_f8f6f4 v[106:109], v[10:17], v[230:237], v[106:109]
	s_setprio 0
	s_setprio 1
	v_mfma_f32_16x16x128_f8f6f4 v[150:153], v[18:25], v[198:205], v[150:153]
	v_mfma_f32_16x16x128_f8f6f4 v[146:149], v[26:33], v[198:205], v[146:149]
	v_mfma_f32_16x16x128_f8f6f4 v[134:137], v[18:25], v[206:213], v[134:137]
	v_mfma_f32_16x16x128_f8f6f4 v[130:133], v[26:33], v[206:213], v[130:133]
	v_mfma_f32_16x16x128_f8f6f4 v[118:121], v[18:25], v[214:221], v[118:121]
	v_mfma_f32_16x16x128_f8f6f4 v[114:117], v[26:33], v[214:221], v[114:117]
	v_mfma_f32_16x16x128_f8f6f4 v[102:105], v[18:25], v[230:237], v[102:105]
	v_mfma_f32_16x16x128_f8f6f4 v[98:101], v[26:33], v[230:237], v[98:101]
	s_setprio 0
	s_barrier
	s_add_i32 s46, s71, s53
	v_lshl_add_u64 v[184:185], v[184:185], 0, s[12:13]
	s_mov_b32 m0, s46
	ds_read_b128 v[198:201], v196 offset:49152
	ds_read_b128 v[202:205], v196 offset:50176
	ds_read_b128 v[206:209], v196 offset:51200
	ds_read_b128 v[210:213], v196 offset:52224
	ds_read_b128 v[214:217], v196 offset:53248
	ds_read_b128 v[218:221], v196 offset:54272
	ds_read_b128 v[230:233], v196 offset:55296
	ds_read_b128 v[234:237], v196 offset:56320
	global_load_lds_dwordx4 v[184:185], off
	s_add_i32 m0, s46, 0x2000
	s_add_u32 s44, s44, 0x40080
	v_lshl_add_u64 v[184:185], v[186:187], 0, s[12:13]
	s_addc_u32 s45, s45, 0
	s_add_i32 s46, s72, s53
	global_load_lds_dwordx4 v[184:185], off
	v_lshl_add_u64 v[184:185], s[44:45], 0, v[162:163]
	s_mov_b32 m0, s46
	s_nop 0
	global_load_lds_dwordx4 v[184:185], off
	v_lshl_add_u64 v[184:185], s[44:45], 0, v[164:165]
	s_add_i32 m0, s46, 0x2000
	s_nop 0
	global_load_lds_dwordx4 v[184:185], off
	v_lshl_add_u64 v[184:185], v[188:189], 0, s[12:13]
	s_mov_b32 m0, s59
	s_nop 0
	global_load_lds_dwordx4 v[184:185], off
	v_lshl_add_u64 v[184:185], v[190:191], 0, s[12:13]
	s_mov_b32 m0, s60
	s_nop 0
	global_load_lds_dwordx4 v[184:185], off
	s_waitcnt vmcnt(8)
	s_waitcnt lgkmcnt(0)
	s_barrier
	s_setprio 1
	s_waitcnt lgkmcnt(0)
	v_mfma_f32_16x16x128_f8f6f4 v[90:93], v[2:9], v[198:205], v[90:93]
	v_mfma_f32_16x16x128_f8f6f4 v[82:85], v[10:17], v[198:205], v[82:85]
	v_mfma_f32_16x16x128_f8f6f4 v[70:73], v[2:9], v[206:213], v[70:73]
	v_mfma_f32_16x16x128_f8f6f4 v[66:69], v[10:17], v[206:213], v[66:69]
	v_mfma_f32_16x16x128_f8f6f4 v[54:57], v[2:9], v[214:221], v[54:57]
	v_mfma_f32_16x16x128_f8f6f4 v[50:53], v[10:17], v[214:221], v[50:53]
	v_mfma_f32_16x16x128_f8f6f4 v[38:41], v[2:9], v[230:237], v[38:41]
	v_mfma_f32_16x16x128_f8f6f4 v[34:37], v[10:17], v[230:237], v[34:37]
	s_setprio 0
	s_setprio 1
	v_mfma_f32_16x16x128_f8f6f4 v[94:97], v[18:25], v[198:205], v[94:97]
	v_mfma_f32_16x16x128_f8f6f4 v[86:89], v[26:33], v[198:205], v[86:89]
	v_mfma_f32_16x16x128_f8f6f4 v[78:81], v[18:25], v[206:213], v[78:81]
	v_mfma_f32_16x16x128_f8f6f4 v[74:77], v[26:33], v[206:213], v[74:77]
	v_mfma_f32_16x16x128_f8f6f4 v[62:65], v[18:25], v[214:221], v[62:65]
	v_mfma_f32_16x16x128_f8f6f4 v[58:61], v[26:33], v[214:221], v[58:61]
	v_mfma_f32_16x16x128_f8f6f4 v[46:49], v[18:25], v[230:237], v[46:49]
	v_mfma_f32_16x16x128_f8f6f4 v[42:45], v[26:33], v[230:237], v[42:45]
	s_setprio 0
	s_barrier
	s_add_i32 s70, s70, 2
	s_add_u32 s42, s42, 0x100
	s_addc_u32 s43, s43, 0
	s_add_u32 s68, s68, 0x100
	s_addc_u32 s69, s69, 0
	s_cmp_gt_u32 s70, 13
	s_cbranch_scc0 .LBB0_460

.LBB0_1346:
	s_ashr_i32 s17, s16, 31
	s_lshl_b64 s[24:25], s[16:17], 16
	s_add_i32 s17, s50, 0x80
	v_add_u32_e32 v202, s17, v1
	v_add_u32_e32 v203, s17, v190
	s_lshl_b32 s17, s16, 2
	s_add_i32 s17, s17, 0
	s_add_i32 s17, s17, 0x20000
	s_add_u32 s24, s18, s24
	s_addc_u32 s25, s19, s25
	v_mov_b32_e32 v175, v167
	v_mov_b32_e32 v173, v167
	s_add_u32 s56, s26, 0x100
	v_add_u32_e32 v200, s50, v1
	v_add_u32_e32 v201, s50, v190
	v_lshl_add_u64 v[178:179], s[10:11], 0, v[172:173]
	v_lshl_add_u64 v[180:181], s[10:11], 0, v[174:175]
	s_addc_u32 s57, s27, 0
	s_mov_b32 s58, -2
	s_mov_b64 s[26:27], 0
	s_xor_b64 s[28:29], s[22:23], -1
	v_mov_b32_e32 v169, v199
	v_mov_b32_e32 v171, v176
	v_mov_b32_e32 v173, v174
	v_mov_b32_e32 v175, v172
	s_add_u32 s30, s84, s26
	s_addc_u32 s31, s85, s27
	v_add_u32_e32 v2, s3, v193
	v_add_u32_e32 v14, s2, v193
	s_add_u32 s34, s30, 0x35400100
	ds_read_b128 v[18:21], v2
	ds_read_b128 v[22:25], v2 offset:1024
	ds_read_b128 v[26:29], v2 offset:2048
	ds_read_b128 v[30:33], v2 offset:3072
	ds_read_b128 v[2:5], v14
	ds_read_b128 v[6:9], v14 offset:1024
	ds_read_b128 v[10:13], v14 offset:2048
	ds_read_b128 v[14:17], v14 offset:3072
	s_addc_u32 s35, s31, 0
	s_add_u32 s59, s56, s26
	s_addc_u32 s60, s57, s27
	s_cmpk_eq_i32 s26, 0x700
	s_cselect_b64 vcc, -1, 0
	s_and_b64 s[30:31], vcc, exec
	v_cndmask_b32_e32 v166, v199, v169, vcc
	s_cselect_b32 s35, s5, s35
	s_cselect_b32 s34, s4, s34
	v_cndmask_b32_e32 v238, v176, v171, vcc
	v_cndmask_b32_e32 v229, v174, v173, vcc
	v_cndmask_b32_e32 v240, v172, v175, vcc
	s_cselect_b32 s31, s21, s60
	s_cselect_b32 s30, s20, s59
	v_lshl_add_u64 v[230:231], v[180:181], 0, s[26:27]
	s_add_i32 m0, s39, 0xc000
	ds_read_b128 v[182:185], v197
	ds_read_b128 v[186:189], v197 offset:1024
	ds_read_b128 v[204:207], v197 offset:2048
	ds_read_b128 v[208:211], v197 offset:3072
	ds_read_b128 v[212:215], v197 offset:4096
	ds_read_b128 v[216:219], v197 offset:5120
	ds_read_b128 v[220:223], v197 offset:6144
	ds_read_b128 v[224:227], v197 offset:7168
	global_load_lds_dwordx4 v[230:231], off
	v_lshl_add_u64 v[230:231], v[178:179], 0, s[26:27]
	s_add_i32 m0, s39, 0xe000
	s_nop 0
	global_load_lds_dwordx4 v[230:231], off
	s_waitcnt vmcnt(8)
	s_waitcnt lgkmcnt(0)
	s_barrier
	s_setprio 1
	s_waitcnt lgkmcnt(0)
	v_mfma_f32_16x16x128_f8f6f4 v[158:161], v[18:25], v[182:189], 0
	v_mfma_f32_16x16x128_f8f6f4 v[150:153], v[26:33], v[182:189], 0
	v_mfma_f32_16x16x128_f8f6f4 v[142:145], v[18:25], v[204:211], 0
	v_mfma_f32_16x16x128_f8f6f4 v[134:137], v[26:33], v[204:211], 0
	v_mfma_f32_16x16x128_f8f6f4 v[126:129], v[18:25], v[212:219], 0
	v_mfma_f32_16x16x128_f8f6f4 v[118:121], v[26:33], v[212:219], 0
	v_mfma_f32_16x16x128_f8f6f4 v[110:113], v[18:25], v[220:227], 0
	v_mfma_f32_16x16x128_f8f6f4 v[102:105], v[26:33], v[220:227], 0
	s_setprio 0
	s_setprio 1
	v_mfma_f32_16x16x128_f8f6f4 v[154:157], v[2:9], v[182:189], 0
	v_mfma_f32_16x16x128_f8f6f4 v[146:149], v[10:17], v[182:189], 0
	v_mfma_f32_16x16x128_f8f6f4 v[138:141], v[2:9], v[204:211], 0
	v_mfma_f32_16x16x128_f8f6f4 v[130:133], v[10:17], v[204:211], 0
	v_mfma_f32_16x16x128_f8f6f4 v[122:125], v[2:9], v[212:219], 0
	v_mfma_f32_16x16x128_f8f6f4 v[114:117], v[10:17], v[212:219], 0
	v_mfma_f32_16x16x128_f8f6f4 v[106:109], v[2:9], v[220:227], 0
	v_mfma_f32_16x16x128_f8f6f4 v[98:101], v[10:17], v[220:227], 0
	s_setprio 0
	s_barrier
	s_add_i32 s59, s3, s38
	v_lshl_add_u64 v[182:183], s[30:31], 0, v[164:165]
	s_mov_b32 m0, s59
	ds_read_b128 v[204:207], v197 offset:16384
	ds_read_b128 v[208:211], v197 offset:17408
	ds_read_b128 v[212:215], v197 offset:18432
	ds_read_b128 v[216:219], v197 offset:19456
	ds_read_b128 v[220:223], v197 offset:20480
	ds_read_b128 v[224:227], v197 offset:21504
	ds_read_b128 v[230:233], v197 offset:22528
	ds_read_b128 v[234:237], v197 offset:23552
	global_load_lds_dwordx4 v[182:183], off
	s_add_i32 m0, s59, 0x2000
	s_add_u32 s60, s30, 0x40000
	v_lshl_add_u64 v[184:185], s[30:31], 0, v[162:163]
	s_addc_u32 s61, s31, 0
	s_add_i32 s59, s2, s38
	global_load_lds_dwordx4 v[184:185], off
	v_lshl_add_u64 v[186:187], s[60:61], 0, v[164:165]
	s_mov_b32 m0, s59
	v_mov_b32_e32 v239, v167
	global_load_lds_dwordx4 v[186:187], off
	v_lshl_add_u64 v[186:187], s[60:61], 0, v[162:163]
	s_add_i32 m0, s59, 0x2000
	v_lshl_add_u64 v[188:189], s[34:35], 0, v[166:167]
	global_load_lds_dwordx4 v[186:187], off
	s_mov_b32 m0, s39
	v_lshl_add_u64 v[186:187], s[34:35], 0, v[238:239]
	global_load_lds_dwordx4 v166, s[34:35]
	s_mov_b32 m0, s40
	s_nop 0
	global_load_lds_dwordx4 v238, s[34:35]
	s_waitcnt vmcnt(8)
	s_waitcnt lgkmcnt(0)
	s_barrier
	s_setprio 1
	s_waitcnt lgkmcnt(0)
	v_mfma_f32_16x16x128_f8f6f4 v[94:97], v[18:25], v[204:211], 0
	v_mfma_f32_16x16x128_f8f6f4 v[86:89], v[26:33], v[204:211], 0
	v_mfma_f32_16x16x128_f8f6f4 v[78:81], v[18:25], v[212:219], 0
	v_mfma_f32_16x16x128_f8f6f4 v[66:69], v[26:33], v[212:219], 0
	v_mfma_f32_16x16x128_f8f6f4 v[54:57], v[18:25], v[220:227], 0
	v_mfma_f32_16x16x128_f8f6f4 v[46:49], v[26:33], v[220:227], 0
	v_mfma_f32_16x16x128_f8f6f4 v[38:41], v[18:25], v[230:237], 0
	v_mfma_f32_16x16x128_f8f6f4 v[34:37], v[26:33], v[230:237], 0
	s_setprio 0
	s_setprio 1
	v_mfma_f32_16x16x128_f8f6f4 v[90:93], v[2:9], v[204:211], 0
	v_mfma_f32_16x16x128_f8f6f4 v[82:85], v[10:17], v[204:211], 0
	v_mfma_f32_16x16x128_f8f6f4 v[74:77], v[2:9], v[212:219], 0
	v_mfma_f32_16x16x128_f8f6f4 v[58:61], v[10:17], v[212:219], 0
	v_mfma_f32_16x16x128_f8f6f4 v[70:73], v[2:9], v[220:227], 0
	v_mfma_f32_16x16x128_f8f6f4 v[62:65], v[10:17], v[220:227], 0
	v_mfma_f32_16x16x128_f8f6f4 v[50:53], v[2:9], v[230:237], 0
	v_mfma_f32_16x16x128_f8f6f4 v[42:45], v[10:17], v[230:237], 0
	s_setprio 0
	s_barrier
	v_add_u32_e32 v14, s86, v193
	v_add_u32_e32 v30, s87, v193
	ds_read_b128 v[2:5], v14
	ds_read_b128 v[6:9], v14 offset:1024
	ds_read_b128 v[10:13], v14 offset:2048
	ds_read_b128 v[14:17], v14 offset:3072
	ds_read_b128 v[18:21], v30
	ds_read_b128 v[22:25], v30 offset:1024
	ds_read_b128 v[26:29], v30 offset:2048
	ds_read_b128 v[30:33], v30 offset:3072
	s_mov_b32 m0, s41
	ds_read_b128 v[204:207], v197 offset:32768
	ds_read_b128 v[208:211], v197 offset:33792
	ds_read_b128 v[212:215], v197 offset:34816
	ds_read_b128 v[216:219], v197 offset:35840
	ds_read_b128 v[220:223], v197 offset:36864
	ds_read_b128 v[224:227], v197 offset:37888
	ds_read_b128 v[230:233], v197 offset:38912
	ds_read_b128 v[234:237], v197 offset:39936
	global_load_lds_dwordx4 v229, s[34:35]
	s_mov_b32 m0, s42
	s_nop 0
	global_load_lds_dwordx4 v240, s[34:35]
	s_waitcnt vmcnt(8)
	s_waitcnt lgkmcnt(0)
	s_barrier
	s_setprio 1
	s_waitcnt lgkmcnt(0)
	v_mfma_f32_16x16x128_f8f6f4 v[158:161], v[2:9], v[204:211], v[158:161]
	v_mfma_f32_16x16x128_f8f6f4 v[150:153], v[10:17], v[204:211], v[150:153]
	v_mfma_f32_16x16x128_f8f6f4 v[142:145], v[2:9], v[212:219], v[142:145]
	v_mfma_f32_16x16x128_f8f6f4 v[134:137], v[10:17], v[212:219], v[134:137]
	v_mfma_f32_16x16x128_f8f6f4 v[126:129], v[2:9], v[220:227], v[126:129]
	v_mfma_f32_16x16x128_f8f6f4 v[118:121], v[10:17], v[220:227], v[118:121]
	v_mfma_f32_16x16x128_f8f6f4 v[110:113], v[2:9], v[230:237], v[110:113]
	v_mfma_f32_16x16x128_f8f6f4 v[102:105], v[10:17], v[230:237], v[102:105]
	s_setprio 0
	s_setprio 1
	v_mfma_f32_16x16x128_f8f6f4 v[154:157], v[18:25], v[204:211], v[154:157]
	v_mfma_f32_16x16x128_f8f6f4 v[146:149], v[26:33], v[204:211], v[146:149]
	v_mfma_f32_16x16x128_f8f6f4 v[138:141], v[18:25], v[212:219], v[138:141]
	v_mfma_f32_16x16x128_f8f6f4 v[130:133], v[26:33], v[212:219], v[130:133]
	v_mfma_f32_16x16x128_f8f6f4 v[122:125], v[18:25], v[220:227], v[122:125]
	v_mfma_f32_16x16x128_f8f6f4 v[114:117], v[26:33], v[220:227], v[114:117]
	v_mfma_f32_16x16x128_f8f6f4 v[106:109], v[18:25], v[230:237], v[106:109]
	v_mfma_f32_16x16x128_f8f6f4 v[98:101], v[26:33], v[230:237], v[98:101]
	s_setprio 0
	s_barrier
	s_add_i32 s34, s86, s38
	v_lshl_add_u64 v[182:183], v[182:183], 0, s[8:9]
	s_mov_b32 m0, s34
	ds_read_b128 v[204:207], v197 offset:49152
	ds_read_b128 v[208:211], v197 offset:50176
	ds_read_b128 v[212:215], v197 offset:51200
	ds_read_b128 v[216:219], v197 offset:52224
	ds_read_b128 v[220:223], v197 offset:53248
	ds_read_b128 v[224:227], v197 offset:54272
	ds_read_b128 v[230:233], v197 offset:55296
	ds_read_b128 v[234:237], v197 offset:56320
	global_load_lds_dwordx4 v[182:183], off
	s_add_i32 m0, s34, 0x2000
	s_add_u32 s30, s30, 0x40080
	v_lshl_add_u64 v[182:183], v[184:185], 0, s[8:9]
	s_addc_u32 s31, s31, 0
	s_add_i32 s34, s87, s38
	global_load_lds_dwordx4 v[182:183], off
	v_lshl_add_u64 v[182:183], s[30:31], 0, v[164:165]
	s_mov_b32 m0, s34
	s_nop 0
	global_load_lds_dwordx4 v[182:183], off
	v_lshl_add_u64 v[182:183], s[30:31], 0, v[162:163]
	s_add_i32 m0, s34, 0x2000
	s_nop 0
	global_load_lds_dwordx4 v[182:183], off
	v_lshl_add_u64 v[182:183], v[188:189], 0, s[8:9]
	s_mov_b32 m0, s43
	s_nop 0
	global_load_lds_dwordx4 v[182:183], off
	v_lshl_add_u64 v[182:183], v[186:187], 0, s[8:9]
	s_mov_b32 m0, s44
	s_nop 0
	global_load_lds_dwordx4 v[182:183], off
	s_waitcnt vmcnt(8)
	s_waitcnt lgkmcnt(0)
	s_barrier
	s_setprio 1
	s_waitcnt lgkmcnt(0)
	v_mfma_f32_16x16x128_f8f6f4 v[94:97], v[2:9], v[204:211], v[94:97]
	v_mfma_f32_16x16x128_f8f6f4 v[86:89], v[10:17], v[204:211], v[86:89]
	v_mfma_f32_16x16x128_f8f6f4 v[78:81], v[2:9], v[212:219], v[78:81]
	v_mfma_f32_16x16x128_f8f6f4 v[66:69], v[10:17], v[212:219], v[66:69]
	v_mfma_f32_16x16x128_f8f6f4 v[54:57], v[2:9], v[220:227], v[54:57]
	v_mfma_f32_16x16x128_f8f6f4 v[46:49], v[10:17], v[220:227], v[46:49]
	v_mfma_f32_16x16x128_f8f6f4 v[38:41], v[2:9], v[230:237], v[38:41]
	v_mfma_f32_16x16x128_f8f6f4 v[34:37], v[10:17], v[230:237], v[34:37]
	s_setprio 0
	s_setprio 1
	v_mfma_f32_16x16x128_f8f6f4 v[90:93], v[18:25], v[204:211], v[90:93]
	v_mfma_f32_16x16x128_f8f6f4 v[82:85], v[26:33], v[204:211], v[82:85]
	v_mfma_f32_16x16x128_f8f6f4 v[74:77], v[18:25], v[212:219], v[74:77]
	v_mfma_f32_16x16x128_f8f6f4 v[58:61], v[26:33], v[212:219], v[58:61]
	v_mfma_f32_16x16x128_f8f6f4 v[70:73], v[18:25], v[220:227], v[70:73]
	v_mfma_f32_16x16x128_f8f6f4 v[62:65], v[26:33], v[220:227], v[62:65]
	v_mfma_f32_16x16x128_f8f6f4 v[50:53], v[18:25], v[230:237], v[50:53]
	v_mfma_f32_16x16x128_f8f6f4 v[42:45], v[26:33], v[230:237], v[42:45]
	s_setprio 0
	s_barrier
	s_add_i32 s58, s58, 2
	s_add_u32 s26, s26, 0x100
	s_addc_u32 s27, s27, 0
	s_cmp_gt_u32 s58, 13
	s_cbranch_scc1 .LBB0_1350
	s_branch .LBB0_1348
.LBB0_1347:
	s_add_u32 s30, s84, s26
	s_addc_u32 s31, s85, s27
	v_add_u32_e32 v2, s3, v193
	v_add_u32_e32 v14, s2, v193
	s_add_u32 s34, s30, 0x35400100
	ds_read_b128 v[18:21], v2
	ds_read_b128 v[22:25], v2 offset:1024
	ds_read_b128 v[26:29], v2 offset:2048
	ds_read_b128 v[30:33], v2 offset:3072
	ds_read_b128 v[2:5], v14
	ds_read_b128 v[6:9], v14 offset:1024
	ds_read_b128 v[10:13], v14 offset:2048
	ds_read_b128 v[14:17], v14 offset:3072
	s_addc_u32 s35, s31, 0
	s_add_u32 s59, s56, s26
	s_addc_u32 s60, s57, s27
	s_cmpk_eq_i32 s26, 0x700
	s_cselect_b64 vcc, -1, 0
	s_and_b64 s[30:31], vcc, exec
	v_cndmask_b32_e32 v166, v199, v169, vcc
	s_cselect_b32 s35, s5, s35
	s_cselect_b32 s34, s4, s34
	v_cndmask_b32_e32 v238, v176, v171, vcc
	v_cndmask_b32_e32 v229, v174, v173, vcc
	v_cndmask_b32_e32 v240, v172, v175, vcc
	s_cselect_b32 s31, s21, s60
	s_cselect_b32 s30, s20, s59
	v_lshl_add_u64 v[230:231], v[180:181], 0, s[26:27]
	s_add_i32 m0, s39, 0xc000
	ds_read_b128 v[182:185], v197
	ds_read_b128 v[186:189], v197 offset:1024
	ds_read_b128 v[204:207], v197 offset:2048
	ds_read_b128 v[208:211], v197 offset:3072
	ds_read_b128 v[212:215], v197 offset:4096
	ds_read_b128 v[216:219], v197 offset:5120
	ds_read_b128 v[220:223], v197 offset:6144
	ds_read_b128 v[224:227], v197 offset:7168
	global_load_lds_dwordx4 v[230:231], off
	v_lshl_add_u64 v[230:231], v[178:179], 0, s[26:27]
	s_add_i32 m0, s39, 0xe000
	s_nop 0
	global_load_lds_dwordx4 v[230:231], off
	s_waitcnt vmcnt(8)
	s_waitcnt lgkmcnt(0)
	s_barrier
	s_setprio 1
	s_waitcnt lgkmcnt(0)
	v_mfma_f32_16x16x128_f8f6f4 v[158:161], v[18:25], v[182:189], v[158:161]
	v_mfma_f32_16x16x128_f8f6f4 v[150:153], v[26:33], v[182:189], v[150:153]
	v_mfma_f32_16x16x128_f8f6f4 v[142:145], v[18:25], v[204:211], v[142:145]
	v_mfma_f32_16x16x128_f8f6f4 v[134:137], v[26:33], v[204:211], v[134:137]
	v_mfma_f32_16x16x128_f8f6f4 v[126:129], v[18:25], v[212:219], v[126:129]
	v_mfma_f32_16x16x128_f8f6f4 v[118:121], v[26:33], v[212:219], v[118:121]
	v_mfma_f32_16x16x128_f8f6f4 v[110:113], v[18:25], v[220:227], v[110:113]
	v_mfma_f32_16x16x128_f8f6f4 v[102:105], v[26:33], v[220:227], v[102:105]
	s_setprio 0
	s_setprio 1
	v_mfma_f32_16x16x128_f8f6f4 v[154:157], v[2:9], v[182:189], v[154:157]
	v_mfma_f32_16x16x128_f8f6f4 v[146:149], v[10:17], v[182:189], v[146:149]
	v_mfma_f32_16x16x128_f8f6f4 v[138:141], v[2:9], v[204:211], v[138:141]
	v_mfma_f32_16x16x128_f8f6f4 v[130:133], v[10:17], v[204:211], v[130:133]
	v_mfma_f32_16x16x128_f8f6f4 v[122:125], v[2:9], v[212:219], v[122:125]
	v_mfma_f32_16x16x128_f8f6f4 v[114:117], v[10:17], v[212:219], v[114:117]
	v_mfma_f32_16x16x128_f8f6f4 v[106:109], v[2:9], v[220:227], v[106:109]
	v_mfma_f32_16x16x128_f8f6f4 v[98:101], v[10:17], v[220:227], v[98:101]
	s_setprio 0
	s_barrier
	s_add_i32 s59, s3, s38
	v_lshl_add_u64 v[182:183], s[30:31], 0, v[164:165]
	s_mov_b32 m0, s59
	ds_read_b128 v[204:207], v197 offset:16384
	ds_read_b128 v[208:211], v197 offset:17408
	ds_read_b128 v[212:215], v197 offset:18432
	ds_read_b128 v[216:219], v197 offset:19456
	ds_read_b128 v[220:223], v197 offset:20480
	ds_read_b128 v[224:227], v197 offset:21504
	ds_read_b128 v[230:233], v197 offset:22528
	ds_read_b128 v[234:237], v197 offset:23552
	global_load_lds_dwordx4 v[182:183], off
	s_add_i32 m0, s59, 0x2000
	s_add_u32 s60, s30, 0x40000
	v_lshl_add_u64 v[184:185], s[30:31], 0, v[162:163]
	s_addc_u32 s61, s31, 0
	s_add_i32 s59, s2, s38
	global_load_lds_dwordx4 v[184:185], off
	v_lshl_add_u64 v[186:187], s[60:61], 0, v[164:165]
	s_mov_b32 m0, s59
	v_mov_b32_e32 v239, v167
	global_load_lds_dwordx4 v[186:187], off
	v_lshl_add_u64 v[186:187], s[60:61], 0, v[162:163]
	s_add_i32 m0, s59, 0x2000
	v_lshl_add_u64 v[188:189], s[34:35], 0, v[166:167]
	global_load_lds_dwordx4 v[186:187], off
	s_mov_b32 m0, s39
	v_lshl_add_u64 v[186:187], s[34:35], 0, v[238:239]
	global_load_lds_dwordx4 v166, s[34:35]
	s_mov_b32 m0, s40
	s_nop 0
	global_load_lds_dwordx4 v238, s[34:35]
	s_waitcnt vmcnt(8)
	s_waitcnt lgkmcnt(0)
	s_barrier
	s_setprio 1
	s_waitcnt lgkmcnt(0)
	v_mfma_f32_16x16x128_f8f6f4 v[94:97], v[18:25], v[204:211], v[94:97]
	v_mfma_f32_16x16x128_f8f6f4 v[86:89], v[26:33], v[204:211], v[86:89]
	v_mfma_f32_16x16x128_f8f6f4 v[78:81], v[18:25], v[212:219], v[78:81]
	v_mfma_f32_16x16x128_f8f6f4 v[66:69], v[26:33], v[212:219], v[66:69]
	v_mfma_f32_16x16x128_f8f6f4 v[54:57], v[18:25], v[220:227], v[54:57]
	v_mfma_f32_16x16x128_f8f6f4 v[46:49], v[26:33], v[220:227], v[46:49]
	v_mfma_f32_16x16x128_f8f6f4 v[38:41], v[18:25], v[230:237], v[38:41]
	v_mfma_f32_16x16x128_f8f6f4 v[34:37], v[26:33], v[230:237], v[34:37]
	s_setprio 0
	s_setprio 1
	v_mfma_f32_16x16x128_f8f6f4 v[90:93], v[2:9], v[204:211], v[90:93]
	v_mfma_f32_16x16x128_f8f6f4 v[82:85], v[10:17], v[204:211], v[82:85]
	v_mfma_f32_16x16x128_f8f6f4 v[74:77], v[2:9], v[212:219], v[74:77]
	v_mfma_f32_16x16x128_f8f6f4 v[58:61], v[10:17], v[212:219], v[58:61]
	v_mfma_f32_16x16x128_f8f6f4 v[70:73], v[2:9], v[220:227], v[70:73]
	v_mfma_f32_16x16x128_f8f6f4 v[62:65], v[10:17], v[220:227], v[62:65]
	v_mfma_f32_16x16x128_f8f6f4 v[50:53], v[2:9], v[230:237], v[50:53]
	v_mfma_f32_16x16x128_f8f6f4 v[42:45], v[10:17], v[230:237], v[42:45]
	s_setprio 0
	s_barrier
	v_add_u32_e32 v14, s86, v193
	v_add_u32_e32 v30, s87, v193
	ds_read_b128 v[2:5], v14
	ds_read_b128 v[6:9], v14 offset:1024
	ds_read_b128 v[10:13], v14 offset:2048
	ds_read_b128 v[14:17], v14 offset:3072
	ds_read_b128 v[18:21], v30
	ds_read_b128 v[22:25], v30 offset:1024
	ds_read_b128 v[26:29], v30 offset:2048
	ds_read_b128 v[30:33], v30 offset:3072
	s_mov_b32 m0, s41
	ds_read_b128 v[204:207], v197 offset:32768
	ds_read_b128 v[208:211], v197 offset:33792
	ds_read_b128 v[212:215], v197 offset:34816
	ds_read_b128 v[216:219], v197 offset:35840
	ds_read_b128 v[220:223], v197 offset:36864
	ds_read_b128 v[224:227], v197 offset:37888
	ds_read_b128 v[230:233], v197 offset:38912
	ds_read_b128 v[234:237], v197 offset:39936
	global_load_lds_dwordx4 v229, s[34:35]
	s_mov_b32 m0, s42
	s_nop 0
	global_load_lds_dwordx4 v240, s[34:35]
	s_waitcnt vmcnt(8)
	s_waitcnt lgkmcnt(0)
	s_barrier
	s_setprio 1
	s_waitcnt lgkmcnt(0)
	v_mfma_f32_16x16x128_f8f6f4 v[158:161], v[2:9], v[204:211], v[158:161]
	v_mfma_f32_16x16x128_f8f6f4 v[150:153], v[10:17], v[204:211], v[150:153]
	v_mfma_f32_16x16x128_f8f6f4 v[142:145], v[2:9], v[212:219], v[142:145]
	v_mfma_f32_16x16x128_f8f6f4 v[134:137], v[10:17], v[212:219], v[134:137]
	v_mfma_f32_16x16x128_f8f6f4 v[126:129], v[2:9], v[220:227], v[126:129]
	v_mfma_f32_16x16x128_f8f6f4 v[118:121], v[10:17], v[220:227], v[118:121]
	v_mfma_f32_16x16x128_f8f6f4 v[110:113], v[2:9], v[230:237], v[110:113]
	v_mfma_f32_16x16x128_f8f6f4 v[102:105], v[10:17], v[230:237], v[102:105]
	s_setprio 0
	s_setprio 1
	v_mfma_f32_16x16x128_f8f6f4 v[154:157], v[18:25], v[204:211], v[154:157]
	v_mfma_f32_16x16x128_f8f6f4 v[146:149], v[26:33], v[204:211], v[146:149]
	v_mfma_f32_16x16x128_f8f6f4 v[138:141], v[18:25], v[212:219], v[138:141]
	v_mfma_f32_16x16x128_f8f6f4 v[130:133], v[26:33], v[212:219], v[130:133]
	v_mfma_f32_16x16x128_f8f6f4 v[122:125], v[18:25], v[220:227], v[122:125]
	v_mfma_f32_16x16x128_f8f6f4 v[114:117], v[26:33], v[220:227], v[114:117]
	v_mfma_f32_16x16x128_f8f6f4 v[106:109], v[18:25], v[230:237], v[106:109]
	v_mfma_f32_16x16x128_f8f6f4 v[98:101], v[26:33], v[230:237], v[98:101]
	s_setprio 0
	s_barrier
	s_add_i32 s34, s86, s38
	v_lshl_add_u64 v[182:183], v[182:183], 0, s[8:9]
	s_mov_b32 m0, s34
	ds_read_b128 v[204:207], v197 offset:49152
	ds_read_b128 v[208:211], v197 offset:50176
	ds_read_b128 v[212:215], v197 offset:51200
	ds_read_b128 v[216:219], v197 offset:52224
	ds_read_b128 v[220:223], v197 offset:53248
	ds_read_b128 v[224:227], v197 offset:54272
	ds_read_b128 v[230:233], v197 offset:55296
	ds_read_b128 v[234:237], v197 offset:56320
	global_load_lds_dwordx4 v[182:183], off
	s_add_i32 m0, s34, 0x2000
	s_add_u32 s30, s30, 0x40080
	v_lshl_add_u64 v[182:183], v[184:185], 0, s[8:9]
	s_addc_u32 s31, s31, 0
	s_add_i32 s34, s87, s38
	global_load_lds_dwordx4 v[182:183], off
	v_lshl_add_u64 v[182:183], s[30:31], 0, v[164:165]
	s_mov_b32 m0, s34
	s_nop 0
	global_load_lds_dwordx4 v[182:183], off
	v_lshl_add_u64 v[182:183], s[30:31], 0, v[162:163]
	s_add_i32 m0, s34, 0x2000
	s_nop 0
	global_load_lds_dwordx4 v[182:183], off
	v_lshl_add_u64 v[182:183], v[188:189], 0, s[8:9]
	s_mov_b32 m0, s43
	s_nop 0
	global_load_lds_dwordx4 v[182:183], off
	v_lshl_add_u64 v[182:183], v[186:187], 0, s[8:9]
	s_mov_b32 m0, s44
	s_nop 0
	global_load_lds_dwordx4 v[182:183], off
	s_waitcnt vmcnt(8)
	s_waitcnt lgkmcnt(0)
	s_barrier
	s_setprio 1
	s_waitcnt lgkmcnt(0)
	v_mfma_f32_16x16x128_f8f6f4 v[94:97], v[2:9], v[204:211], v[94:97]
	v_mfma_f32_16x16x128_f8f6f4 v[86:89], v[10:17], v[204:211], v[86:89]
	v_mfma_f32_16x16x128_f8f6f4 v[78:81], v[2:9], v[212:219], v[78:81]
	v_mfma_f32_16x16x128_f8f6f4 v[66:69], v[10:17], v[212:219], v[66:69]
	v_mfma_f32_16x16x128_f8f6f4 v[54:57], v[2:9], v[220:227], v[54:57]
	v_mfma_f32_16x16x128_f8f6f4 v[46:49], v[10:17], v[220:227], v[46:49]
	v_mfma_f32_16x16x128_f8f6f4 v[38:41], v[2:9], v[230:237], v[38:41]
	v_mfma_f32_16x16x128_f8f6f4 v[34:37], v[10:17], v[230:237], v[34:37]
	s_setprio 0
	s_setprio 1
	v_mfma_f32_16x16x128_f8f6f4 v[90:93], v[18:25], v[204:211], v[90:93]
	v_mfma_f32_16x16x128_f8f6f4 v[82:85], v[26:33], v[204:211], v[82:85]
	v_mfma_f32_16x16x128_f8f6f4 v[74:77], v[18:25], v[212:219], v[74:77]
	v_mfma_f32_16x16x128_f8f6f4 v[58:61], v[26:33], v[212:219], v[58:61]
	v_mfma_f32_16x16x128_f8f6f4 v[70:73], v[18:25], v[220:227], v[70:73]
	v_mfma_f32_16x16x128_f8f6f4 v[62:65], v[26:33], v[220:227], v[62:65]
	v_mfma_f32_16x16x128_f8f6f4 v[50:53], v[18:25], v[230:237], v[50:53]
	v_mfma_f32_16x16x128_f8f6f4 v[42:45], v[26:33], v[230:237], v[42:45]
	s_setprio 0
	s_barrier
	s_add_i32 s58, s58, 2
	s_add_u32 s26, s26, 0x100
	s_addc_u32 s27, s27, 0
	s_cmp_gt_u32 s58, 13
	s_cbranch_scc1 .LBB0_1350

.LBB0_1418:
	s_add_u32 s26, s26, 0x80
	s_addc_u32 s27, s27, 0
	s_add_u32 s34, s30, 0x100
	s_addc_u32 s35, s31, 0
	s_mov_b32 s50, -2
	ds_read_b128 v[18:21], v192
	ds_read_b128 v[22:25], v192 offset:1024
	ds_read_b128 v[26:29], v192 offset:2048
	ds_read_b128 v[30:33], v192 offset:3072
	ds_read_b128 v[2:5], v193
	ds_read_b128 v[6:9], v193 offset:1024
	ds_read_b128 v[10:13], v193 offset:2048
	ds_read_b128 v[14:17], v193 offset:3072
	s_add_u32 s28, s26, 0x80
	s_addc_u32 s29, s27, 0
	s_cmp_eq_u32 s50, 12
	s_cselect_b32 s31, s19, s29
	s_cselect_b32 s30, s18, s28
	s_cselect_b32 s29, s21, s35
	s_cselect_b32 s28, s20, s34
	v_lshl_add_u64 v[220:221], s[26:27], 0, v[178:179]
	s_add_i32 m0, s38, 0xc000
	ds_read_b128 v[180:183], v194
	ds_read_b128 v[184:187], v194 offset:1024
	ds_read_b128 v[196:199], v194 offset:2048
	ds_read_b128 v[200:203], v194 offset:3072
	ds_read_b128 v[204:207], v194 offset:4096
	ds_read_b128 v[208:211], v194 offset:5120
	ds_read_b128 v[212:215], v194 offset:6144
	ds_read_b128 v[216:219], v194 offset:7168
	global_load_lds_dwordx4 v[220:221], off
	v_lshl_add_u64 v[220:221], s[26:27], 0, v[176:177]
	s_add_i32 m0, s38, 0xe000
	s_nop 0
	global_load_lds_dwordx4 v[220:221], off
	s_waitcnt vmcnt(8)
	s_waitcnt lgkmcnt(0)
	s_barrier
	s_setprio 1
	s_waitcnt lgkmcnt(0)
	v_mfma_f32_16x16x128_f8f6f4 v[158:161], v[18:25], v[180:187], 0
	v_mfma_f32_16x16x128_f8f6f4 v[154:157], v[26:33], v[180:187], 0
	v_mfma_f32_16x16x128_f8f6f4 v[142:145], v[18:25], v[196:203], 0
	v_mfma_f32_16x16x128_f8f6f4 v[138:141], v[26:33], v[196:203], 0
	v_mfma_f32_16x16x128_f8f6f4 v[126:129], v[18:25], v[204:211], 0
	v_mfma_f32_16x16x128_f8f6f4 v[122:125], v[26:33], v[204:211], 0
	v_mfma_f32_16x16x128_f8f6f4 v[110:113], v[18:25], v[212:219], 0
	v_mfma_f32_16x16x128_f8f6f4 v[106:109], v[26:33], v[212:219], 0
	s_setprio 0
	s_setprio 1
	v_mfma_f32_16x16x128_f8f6f4 v[150:153], v[2:9], v[180:187], 0
	v_mfma_f32_16x16x128_f8f6f4 v[146:149], v[10:17], v[180:187], 0
	v_mfma_f32_16x16x128_f8f6f4 v[134:137], v[2:9], v[196:203], 0
	v_mfma_f32_16x16x128_f8f6f4 v[130:133], v[10:17], v[196:203], 0
	v_mfma_f32_16x16x128_f8f6f4 v[118:121], v[2:9], v[204:211], 0
	v_mfma_f32_16x16x128_f8f6f4 v[114:117], v[10:17], v[204:211], 0
	v_mfma_f32_16x16x128_f8f6f4 v[94:97], v[2:9], v[212:219], 0
	v_mfma_f32_16x16x128_f8f6f4 v[90:93], v[10:17], v[212:219], 0
	s_setprio 0
	s_barrier
	s_add_i32 s51, s3, s37
	v_lshl_add_u64 v[180:181], s[28:29], 0, v[164:165]
	s_mov_b32 m0, s51
	ds_read_b128 v[196:199], v194 offset:16384
	ds_read_b128 v[200:203], v194 offset:17408
	ds_read_b128 v[204:207], v194 offset:18432
	ds_read_b128 v[208:211], v194 offset:19456
	ds_read_b128 v[212:215], v194 offset:20480
	ds_read_b128 v[216:219], v194 offset:21504
	ds_read_b128 v[220:223], v194 offset:22528
	ds_read_b128 v[224:227], v194 offset:23552
	global_load_lds_dwordx4 v[180:181], off
	s_add_i32 m0, s51, 0x2000
	s_add_u32 s52, s28, 0x40000
	v_lshl_add_u64 v[182:183], s[28:29], 0, v[162:163]
	s_addc_u32 s53, s29, 0
	s_add_i32 s51, s2, s37
	global_load_lds_dwordx4 v[182:183], off
	v_lshl_add_u64 v[184:185], s[52:53], 0, v[164:165]
	s_mov_b32 m0, s51
	v_lshl_add_u64 v[186:187], s[30:31], 0, v[168:169]
	global_load_lds_dwordx4 v[184:185], off
	v_lshl_add_u64 v[184:185], s[52:53], 0, v[162:163]
	s_add_i32 m0, s51, 0x2000
	s_nop 0
	global_load_lds_dwordx4 v[184:185], off
	v_lshl_add_u64 v[184:185], s[30:31], 0, v[166:167]
	s_mov_b32 m0, s38
	s_nop 0
	global_load_lds_dwordx4 v[184:185], off
	s_mov_b32 m0, s39
	s_nop 0
	global_load_lds_dwordx4 v[186:187], off
	s_waitcnt vmcnt(8)
	s_waitcnt lgkmcnt(0)
	s_barrier
	s_setprio 1
	s_waitcnt lgkmcnt(0)
	v_mfma_f32_16x16x128_f8f6f4 v[78:81], v[18:25], v[196:203], 0
	v_mfma_f32_16x16x128_f8f6f4 v[74:77], v[26:33], v[196:203], 0
	v_mfma_f32_16x16x128_f8f6f4 v[62:65], v[18:25], v[204:211], 0
	v_mfma_f32_16x16x128_f8f6f4 v[58:61], v[26:33], v[204:211], 0
	v_mfma_f32_16x16x128_f8f6f4 v[46:49], v[18:25], v[212:219], 0
	v_mfma_f32_16x16x128_f8f6f4 v[42:45], v[26:33], v[212:219], 0
	v_mfma_f32_16x16x128_f8f6f4 v[38:41], v[18:25], v[220:227], 0
	v_mfma_f32_16x16x128_f8f6f4 v[34:37], v[26:33], v[220:227], 0
	s_setprio 0
	s_setprio 1
	v_mfma_f32_16x16x128_f8f6f4 v[98:101], v[2:9], v[196:203], 0
	v_mfma_f32_16x16x128_f8f6f4 v[102:105], v[10:17], v[196:203], 0
	v_mfma_f32_16x16x128_f8f6f4 v[82:85], v[2:9], v[204:211], 0
	v_mfma_f32_16x16x128_f8f6f4 v[86:89], v[10:17], v[204:211], 0
	v_mfma_f32_16x16x128_f8f6f4 v[66:69], v[2:9], v[212:219], 0
	v_mfma_f32_16x16x128_f8f6f4 v[70:73], v[10:17], v[212:219], 0
	v_mfma_f32_16x16x128_f8f6f4 v[50:53], v[2:9], v[220:227], 0
	v_mfma_f32_16x16x128_f8f6f4 v[54:57], v[10:17], v[220:227], 0
	s_setprio 0
	s_barrier
	v_add_u32_e32 v14, s86, v188
	v_add_u32_e32 v30, s87, v188
	ds_read_b128 v[2:5], v14
	ds_read_b128 v[6:9], v14 offset:1024
	ds_read_b128 v[10:13], v14 offset:2048
	ds_read_b128 v[14:17], v14 offset:3072
	ds_read_b128 v[18:21], v30
	ds_read_b128 v[22:25], v30 offset:1024
	ds_read_b128 v[26:29], v30 offset:2048
	ds_read_b128 v[30:33], v30 offset:3072
	s_mov_b32 m0, s40
	v_lshl_add_u64 v[230:231], s[30:31], 0, v[170:171]
	ds_read_b128 v[196:199], v194 offset:32768
	ds_read_b128 v[200:203], v194 offset:33792
	ds_read_b128 v[204:207], v194 offset:34816
	ds_read_b128 v[208:211], v194 offset:35840
	ds_read_b128 v[212:215], v194 offset:36864
	ds_read_b128 v[216:219], v194 offset:37888
	ds_read_b128 v[220:223], v194 offset:38912
	ds_read_b128 v[224:227], v194 offset:39936
	global_load_lds_dwordx4 v[230:231], off
	v_lshl_add_u64 v[230:231], s[30:31], 0, v[172:173]
	s_mov_b32 m0, s41
	s_nop 0
	global_load_lds_dwordx4 v[230:231], off
	s_waitcnt vmcnt(8)
	s_waitcnt lgkmcnt(0)
	s_barrier
	s_setprio 1
	s_waitcnt lgkmcnt(0)
	v_mfma_f32_16x16x128_f8f6f4 v[158:161], v[2:9], v[196:203], v[158:161]
	v_mfma_f32_16x16x128_f8f6f4 v[154:157], v[10:17], v[196:203], v[154:157]
	v_mfma_f32_16x16x128_f8f6f4 v[142:145], v[2:9], v[204:211], v[142:145]
	v_mfma_f32_16x16x128_f8f6f4 v[138:141], v[10:17], v[204:211], v[138:141]
	v_mfma_f32_16x16x128_f8f6f4 v[126:129], v[2:9], v[212:219], v[126:129]
	v_mfma_f32_16x16x128_f8f6f4 v[122:125], v[10:17], v[212:219], v[122:125]
	v_mfma_f32_16x16x128_f8f6f4 v[110:113], v[2:9], v[220:227], v[110:113]
	v_mfma_f32_16x16x128_f8f6f4 v[106:109], v[10:17], v[220:227], v[106:109]
	s_setprio 0
	s_setprio 1
	v_mfma_f32_16x16x128_f8f6f4 v[150:153], v[18:25], v[196:203], v[150:153]
	v_mfma_f32_16x16x128_f8f6f4 v[146:149], v[26:33], v[196:203], v[146:149]
	v_mfma_f32_16x16x128_f8f6f4 v[134:137], v[18:25], v[204:211], v[134:137]
	v_mfma_f32_16x16x128_f8f6f4 v[130:133], v[26:33], v[204:211], v[130:133]
	v_mfma_f32_16x16x128_f8f6f4 v[118:121], v[18:25], v[212:219], v[118:121]
	v_mfma_f32_16x16x128_f8f6f4 v[114:117], v[26:33], v[212:219], v[114:117]
	v_mfma_f32_16x16x128_f8f6f4 v[94:97], v[18:25], v[220:227], v[94:97]
	v_mfma_f32_16x16x128_f8f6f4 v[90:93], v[26:33], v[220:227], v[90:93]
	s_setprio 0
	s_barrier
	s_add_i32 s30, s86, s37
	v_lshl_add_u64 v[180:181], v[180:181], 0, s[8:9]
	s_mov_b32 m0, s30
	ds_read_b128 v[196:199], v194 offset:49152
	ds_read_b128 v[200:203], v194 offset:50176
	ds_read_b128 v[204:207], v194 offset:51200
	ds_read_b128 v[208:211], v194 offset:52224
	ds_read_b128 v[212:215], v194 offset:53248
	ds_read_b128 v[216:219], v194 offset:54272
	ds_read_b128 v[220:223], v194 offset:55296
	ds_read_b128 v[224:227], v194 offset:56320
	global_load_lds_dwordx4 v[180:181], off
	s_add_i32 m0, s30, 0x2000
	s_add_u32 s28, s28, 0x40080
	v_lshl_add_u64 v[180:181], v[182:183], 0, s[8:9]
	s_addc_u32 s29, s29, 0
	s_add_i32 s30, s87, s37
	global_load_lds_dwordx4 v[180:181], off
	v_lshl_add_u64 v[180:181], s[28:29], 0, v[164:165]
	s_mov_b32 m0, s30
	s_nop 0
	global_load_lds_dwordx4 v[180:181], off
	v_lshl_add_u64 v[180:181], s[28:29], 0, v[162:163]
	s_add_i32 m0, s30, 0x2000
	s_nop 0
	global_load_lds_dwordx4 v[180:181], off
	v_lshl_add_u64 v[180:181], v[184:185], 0, s[8:9]
	s_mov_b32 m0, s43
	s_nop 0
	global_load_lds_dwordx4 v[180:181], off
	v_lshl_add_u64 v[180:181], v[186:187], 0, s[8:9]
	s_mov_b32 m0, s44
	s_nop 0
	global_load_lds_dwordx4 v[180:181], off
	s_waitcnt vmcnt(8)
	s_waitcnt lgkmcnt(0)
	s_barrier
	s_setprio 1
	s_waitcnt lgkmcnt(0)
	v_mfma_f32_16x16x128_f8f6f4 v[78:81], v[2:9], v[196:203], v[78:81]
	v_mfma_f32_16x16x128_f8f6f4 v[74:77], v[10:17], v[196:203], v[74:77]
	v_mfma_f32_16x16x128_f8f6f4 v[62:65], v[2:9], v[204:211], v[62:65]
	v_mfma_f32_16x16x128_f8f6f4 v[58:61], v[10:17], v[204:211], v[58:61]
	v_mfma_f32_16x16x128_f8f6f4 v[46:49], v[2:9], v[212:219], v[46:49]
	v_mfma_f32_16x16x128_f8f6f4 v[42:45], v[10:17], v[212:219], v[42:45]
	v_mfma_f32_16x16x128_f8f6f4 v[38:41], v[2:9], v[220:227], v[38:41]
	v_mfma_f32_16x16x128_f8f6f4 v[34:37], v[10:17], v[220:227], v[34:37]
	s_setprio 0
	s_setprio 1
	v_mfma_f32_16x16x128_f8f6f4 v[98:101], v[18:25], v[196:203], v[98:101]
	v_mfma_f32_16x16x128_f8f6f4 v[102:105], v[26:33], v[196:203], v[102:105]
	v_mfma_f32_16x16x128_f8f6f4 v[82:85], v[18:25], v[204:211], v[82:85]
	v_mfma_f32_16x16x128_f8f6f4 v[86:89], v[26:33], v[204:211], v[86:89]
	v_mfma_f32_16x16x128_f8f6f4 v[66:69], v[18:25], v[212:219], v[66:69]
	v_mfma_f32_16x16x128_f8f6f4 v[70:73], v[26:33], v[212:219], v[70:73]
	v_mfma_f32_16x16x128_f8f6f4 v[50:53], v[18:25], v[220:227], v[50:53]
	v_mfma_f32_16x16x128_f8f6f4 v[54:57], v[26:33], v[220:227], v[54:57]
	s_setprio 0
	s_barrier
	s_add_i32 s50, s50, 2
	s_add_u32 s26, s26, 0x100
	s_addc_u32 s27, s27, 0
	s_add_u32 s34, s34, 0x100
	s_addc_u32 s35, s35, 0
	s_cmp_gt_u32 s50, 13
	s_cbranch_scc0 .LBB0_1419
	s_branch .Lmy_pexit_p9
.LBB0_1419:
	ds_read_b128 v[18:21], v192
	ds_read_b128 v[22:25], v192 offset:1024
	ds_read_b128 v[26:29], v192 offset:2048
	ds_read_b128 v[30:33], v192 offset:3072
	ds_read_b128 v[2:5], v193
	ds_read_b128 v[6:9], v193 offset:1024
	ds_read_b128 v[10:13], v193 offset:2048
	ds_read_b128 v[14:17], v193 offset:3072
	s_add_u32 s28, s26, 0x80
	s_addc_u32 s29, s27, 0
	s_cmp_eq_u32 s50, 12
	s_cselect_b32 s31, s19, s29
	s_cselect_b32 s30, s18, s28
	s_cselect_b32 s29, s21, s35
	s_cselect_b32 s28, s20, s34
	v_lshl_add_u64 v[220:221], s[26:27], 0, v[178:179]
	s_add_i32 m0, s38, 0xc000
	ds_read_b128 v[180:183], v194
	ds_read_b128 v[184:187], v194 offset:1024
	ds_read_b128 v[196:199], v194 offset:2048
	ds_read_b128 v[200:203], v194 offset:3072
	ds_read_b128 v[204:207], v194 offset:4096
	ds_read_b128 v[208:211], v194 offset:5120
	ds_read_b128 v[212:215], v194 offset:6144
	ds_read_b128 v[216:219], v194 offset:7168
	global_load_lds_dwordx4 v[220:221], off
	v_lshl_add_u64 v[220:221], s[26:27], 0, v[176:177]
	s_add_i32 m0, s38, 0xe000
	s_nop 0
	global_load_lds_dwordx4 v[220:221], off
	s_waitcnt vmcnt(8)
	s_waitcnt lgkmcnt(0)
	s_barrier
	s_setprio 1
	s_waitcnt lgkmcnt(0)
	v_mfma_f32_16x16x128_f8f6f4 v[158:161], v[18:25], v[180:187], v[158:161]
	v_mfma_f32_16x16x128_f8f6f4 v[154:157], v[26:33], v[180:187], v[154:157]
	v_mfma_f32_16x16x128_f8f6f4 v[142:145], v[18:25], v[196:203], v[142:145]
	v_mfma_f32_16x16x128_f8f6f4 v[138:141], v[26:33], v[196:203], v[138:141]
	v_mfma_f32_16x16x128_f8f6f4 v[126:129], v[18:25], v[204:211], v[126:129]
	v_mfma_f32_16x16x128_f8f6f4 v[122:125], v[26:33], v[204:211], v[122:125]
	v_mfma_f32_16x16x128_f8f6f4 v[110:113], v[18:25], v[212:219], v[110:113]
	v_mfma_f32_16x16x128_f8f6f4 v[106:109], v[26:33], v[212:219], v[106:109]
	s_setprio 0
	s_setprio 1
	v_mfma_f32_16x16x128_f8f6f4 v[150:153], v[2:9], v[180:187], v[150:153]
	v_mfma_f32_16x16x128_f8f6f4 v[146:149], v[10:17], v[180:187], v[146:149]
	v_mfma_f32_16x16x128_f8f6f4 v[134:137], v[2:9], v[196:203], v[134:137]
	v_mfma_f32_16x16x128_f8f6f4 v[130:133], v[10:17], v[196:203], v[130:133]
	v_mfma_f32_16x16x128_f8f6f4 v[118:121], v[2:9], v[204:211], v[118:121]
	v_mfma_f32_16x16x128_f8f6f4 v[114:117], v[10:17], v[204:211], v[114:117]
	v_mfma_f32_16x16x128_f8f6f4 v[94:97], v[2:9], v[212:219], v[94:97]
	v_mfma_f32_16x16x128_f8f6f4 v[90:93], v[10:17], v[212:219], v[90:93]
	s_setprio 0
	s_barrier
	s_add_i32 s51, s3, s37
	v_lshl_add_u64 v[180:181], s[28:29], 0, v[164:165]
	s_mov_b32 m0, s51
	ds_read_b128 v[196:199], v194 offset:16384
	ds_read_b128 v[200:203], v194 offset:17408
	ds_read_b128 v[204:207], v194 offset:18432
	ds_read_b128 v[208:211], v194 offset:19456
	ds_read_b128 v[212:215], v194 offset:20480
	ds_read_b128 v[216:219], v194 offset:21504
	ds_read_b128 v[220:223], v194 offset:22528
	ds_read_b128 v[224:227], v194 offset:23552
	global_load_lds_dwordx4 v[180:181], off
	s_add_i32 m0, s51, 0x2000
	s_add_u32 s52, s28, 0x40000
	v_lshl_add_u64 v[182:183], s[28:29], 0, v[162:163]
	s_addc_u32 s53, s29, 0
	s_add_i32 s51, s2, s37
	global_load_lds_dwordx4 v[182:183], off
	v_lshl_add_u64 v[184:185], s[52:53], 0, v[164:165]
	s_mov_b32 m0, s51
	v_lshl_add_u64 v[186:187], s[30:31], 0, v[168:169]
	global_load_lds_dwordx4 v[184:185], off
	v_lshl_add_u64 v[184:185], s[52:53], 0, v[162:163]
	s_add_i32 m0, s51, 0x2000
	s_nop 0
	global_load_lds_dwordx4 v[184:185], off
	v_lshl_add_u64 v[184:185], s[30:31], 0, v[166:167]
	s_mov_b32 m0, s38
	s_nop 0
	global_load_lds_dwordx4 v[184:185], off
	s_mov_b32 m0, s39
	s_nop 0
	global_load_lds_dwordx4 v[186:187], off
	s_waitcnt vmcnt(8)
	s_waitcnt lgkmcnt(0)
	s_barrier
	s_setprio 1
	s_waitcnt lgkmcnt(0)
	v_mfma_f32_16x16x128_f8f6f4 v[78:81], v[18:25], v[196:203], v[78:81]
	v_mfma_f32_16x16x128_f8f6f4 v[74:77], v[26:33], v[196:203], v[74:77]
	v_mfma_f32_16x16x128_f8f6f4 v[62:65], v[18:25], v[204:211], v[62:65]
	v_mfma_f32_16x16x128_f8f6f4 v[58:61], v[26:33], v[204:211], v[58:61]
	v_mfma_f32_16x16x128_f8f6f4 v[46:49], v[18:25], v[212:219], v[46:49]
	v_mfma_f32_16x16x128_f8f6f4 v[42:45], v[26:33], v[212:219], v[42:45]
	v_mfma_f32_16x16x128_f8f6f4 v[38:41], v[18:25], v[220:227], v[38:41]
	v_mfma_f32_16x16x128_f8f6f4 v[34:37], v[26:33], v[220:227], v[34:37]
	s_setprio 0
	s_setprio 1
	v_mfma_f32_16x16x128_f8f6f4 v[98:101], v[2:9], v[196:203], v[98:101]
	v_mfma_f32_16x16x128_f8f6f4 v[102:105], v[10:17], v[196:203], v[102:105]
	v_mfma_f32_16x16x128_f8f6f4 v[82:85], v[2:9], v[204:211], v[82:85]
	v_mfma_f32_16x16x128_f8f6f4 v[86:89], v[10:17], v[204:211], v[86:89]
	v_mfma_f32_16x16x128_f8f6f4 v[66:69], v[2:9], v[212:219], v[66:69]
	v_mfma_f32_16x16x128_f8f6f4 v[70:73], v[10:17], v[212:219], v[70:73]
	v_mfma_f32_16x16x128_f8f6f4 v[50:53], v[2:9], v[220:227], v[50:53]
	v_mfma_f32_16x16x128_f8f6f4 v[54:57], v[10:17], v[220:227], v[54:57]
	s_setprio 0
	s_barrier
	v_add_u32_e32 v14, s86, v188
	v_add_u32_e32 v30, s87, v188
	ds_read_b128 v[2:5], v14
	ds_read_b128 v[6:9], v14 offset:1024
	ds_read_b128 v[10:13], v14 offset:2048
	ds_read_b128 v[14:17], v14 offset:3072
	ds_read_b128 v[18:21], v30
	ds_read_b128 v[22:25], v30 offset:1024
	ds_read_b128 v[26:29], v30 offset:2048
	ds_read_b128 v[30:33], v30 offset:3072
	s_mov_b32 m0, s40
	v_lshl_add_u64 v[230:231], s[30:31], 0, v[170:171]
	ds_read_b128 v[196:199], v194 offset:32768
	ds_read_b128 v[200:203], v194 offset:33792
	ds_read_b128 v[204:207], v194 offset:34816
	ds_read_b128 v[208:211], v194 offset:35840
	ds_read_b128 v[212:215], v194 offset:36864
	ds_read_b128 v[216:219], v194 offset:37888
	ds_read_b128 v[220:223], v194 offset:38912
	ds_read_b128 v[224:227], v194 offset:39936
	global_load_lds_dwordx4 v[230:231], off
	v_lshl_add_u64 v[230:231], s[30:31], 0, v[172:173]
	s_mov_b32 m0, s41
	s_nop 0
	global_load_lds_dwordx4 v[230:231], off
	s_waitcnt vmcnt(8)
	s_waitcnt lgkmcnt(0)
	s_barrier
	s_setprio 1
	s_waitcnt lgkmcnt(0)
	v_mfma_f32_16x16x128_f8f6f4 v[158:161], v[2:9], v[196:203], v[158:161]
	v_mfma_f32_16x16x128_f8f6f4 v[154:157], v[10:17], v[196:203], v[154:157]
	v_mfma_f32_16x16x128_f8f6f4 v[142:145], v[2:9], v[204:211], v[142:145]
	v_mfma_f32_16x16x128_f8f6f4 v[138:141], v[10:17], v[204:211], v[138:141]
	v_mfma_f32_16x16x128_f8f6f4 v[126:129], v[2:9], v[212:219], v[126:129]
	v_mfma_f32_16x16x128_f8f6f4 v[122:125], v[10:17], v[212:219], v[122:125]
	v_mfma_f32_16x16x128_f8f6f4 v[110:113], v[2:9], v[220:227], v[110:113]
	v_mfma_f32_16x16x128_f8f6f4 v[106:109], v[10:17], v[220:227], v[106:109]
	s_setprio 0
	s_setprio 1
	v_mfma_f32_16x16x128_f8f6f4 v[150:153], v[18:25], v[196:203], v[150:153]
	v_mfma_f32_16x16x128_f8f6f4 v[146:149], v[26:33], v[196:203], v[146:149]
	v_mfma_f32_16x16x128_f8f6f4 v[134:137], v[18:25], v[204:211], v[134:137]
	v_mfma_f32_16x16x128_f8f6f4 v[130:133], v[26:33], v[204:211], v[130:133]
	v_mfma_f32_16x16x128_f8f6f4 v[118:121], v[18:25], v[212:219], v[118:121]
	v_mfma_f32_16x16x128_f8f6f4 v[114:117], v[26:33], v[212:219], v[114:117]
	v_mfma_f32_16x16x128_f8f6f4 v[94:97], v[18:25], v[220:227], v[94:97]
	v_mfma_f32_16x16x128_f8f6f4 v[90:93], v[26:33], v[220:227], v[90:93]
	s_setprio 0
	s_barrier
	s_add_i32 s30, s86, s37
	v_lshl_add_u64 v[180:181], v[180:181], 0, s[8:9]
	s_mov_b32 m0, s30
	ds_read_b128 v[196:199], v194 offset:49152
	ds_read_b128 v[200:203], v194 offset:50176
	ds_read_b128 v[204:207], v194 offset:51200
	ds_read_b128 v[208:211], v194 offset:52224
	ds_read_b128 v[212:215], v194 offset:53248
	ds_read_b128 v[216:219], v194 offset:54272
	ds_read_b128 v[220:223], v194 offset:55296
	ds_read_b128 v[224:227], v194 offset:56320
	global_load_lds_dwordx4 v[180:181], off
	s_add_i32 m0, s30, 0x2000
	s_add_u32 s28, s28, 0x40080
	v_lshl_add_u64 v[180:181], v[182:183], 0, s[8:9]
	s_addc_u32 s29, s29, 0
	s_add_i32 s30, s87, s37
	global_load_lds_dwordx4 v[180:181], off
	v_lshl_add_u64 v[180:181], s[28:29], 0, v[164:165]
	s_mov_b32 m0, s30
	s_nop 0
	global_load_lds_dwordx4 v[180:181], off
	v_lshl_add_u64 v[180:181], s[28:29], 0, v[162:163]
	s_add_i32 m0, s30, 0x2000
	s_nop 0
	global_load_lds_dwordx4 v[180:181], off
	v_lshl_add_u64 v[180:181], v[184:185], 0, s[8:9]
	s_mov_b32 m0, s43
	s_nop 0
	global_load_lds_dwordx4 v[180:181], off
	v_lshl_add_u64 v[180:181], v[186:187], 0, s[8:9]
	s_mov_b32 m0, s44
	s_nop 0
	global_load_lds_dwordx4 v[180:181], off
	s_waitcnt vmcnt(8)
	s_waitcnt lgkmcnt(0)
	s_barrier
	s_setprio 1
	s_waitcnt lgkmcnt(0)
	v_mfma_f32_16x16x128_f8f6f4 v[78:81], v[2:9], v[196:203], v[78:81]
	v_mfma_f32_16x16x128_f8f6f4 v[74:77], v[10:17], v[196:203], v[74:77]
	v_mfma_f32_16x16x128_f8f6f4 v[62:65], v[2:9], v[204:211], v[62:65]
	v_mfma_f32_16x16x128_f8f6f4 v[58:61], v[10:17], v[204:211], v[58:61]
	v_mfma_f32_16x16x128_f8f6f4 v[46:49], v[2:9], v[212:219], v[46:49]
	v_mfma_f32_16x16x128_f8f6f4 v[42:45], v[10:17], v[212:219], v[42:45]
	v_mfma_f32_16x16x128_f8f6f4 v[38:41], v[2:9], v[220:227], v[38:41]
	v_mfma_f32_16x16x128_f8f6f4 v[34:37], v[10:17], v[220:227], v[34:37]
	s_setprio 0
	s_setprio 1
	v_mfma_f32_16x16x128_f8f6f4 v[98:101], v[18:25], v[196:203], v[98:101]
	v_mfma_f32_16x16x128_f8f6f4 v[102:105], v[26:33], v[196:203], v[102:105]
	v_mfma_f32_16x16x128_f8f6f4 v[82:85], v[18:25], v[204:211], v[82:85]
	v_mfma_f32_16x16x128_f8f6f4 v[86:89], v[26:33], v[204:211], v[86:89]
	v_mfma_f32_16x16x128_f8f6f4 v[66:69], v[18:25], v[212:219], v[66:69]
	v_mfma_f32_16x16x128_f8f6f4 v[70:73], v[26:33], v[212:219], v[70:73]
	v_mfma_f32_16x16x128_f8f6f4 v[50:53], v[18:25], v[220:227], v[50:53]
	v_mfma_f32_16x16x128_f8f6f4 v[54:57], v[26:33], v[220:227], v[54:57]
	s_setprio 0
	s_barrier
	s_add_i32 s50, s50, 2
	s_add_u32 s26, s26, 0x100
	s_addc_u32 s27, s27, 0
	s_add_u32 s34, s34, 0x100
	s_addc_u32 s35, s35, 0
	s_cmp_gt_u32 s50, 13
	s_cbranch_scc0 .LBB0_1419
